# retention Y section: the zero-lookahead 12-MFMA chain reads its V fragments three MFMAs ahead through rotating quads (counted waits)
# baseline (speedup 1.0000x reference)
; #define LAS __attribute__((address_space(3)))
; __device__ __forceinline__ bf16x8 pack8(const float (&f)[8]) { u32x4 u; u.x = cvtpk(f[0], f[1]); u.y = cvtpk(f[2], f[3]); u.z = cvtpk(f[4], f[5]); u.w = cvtpk(f[6], f[7]); return __builtin_bit_cast(bf16x8, u); }
; __device__ __forceinline__ void kv_store(LAS unsigned char* lds, const KVRaw& R, int tid) {
; #pragma unroll
;     for (int i = 0; i < 2; ++i) {
;         const int q2 = tid + 512 * i, row = q2 >> 3, pc = q2 & 7;
;         float fa[8], fb[8], o1[8], o2[8];
;         unpack8(R.ka[i], fa); unpack8(R.kb[i], fb);
;         const float cs[8] = {R.c0[i].x, R.c0[i].y, R.c0[i].z, R.c0[i].w, R.c1[i].x, R.c1[i].y, R.c1[i].z, R.c1[i].w}, sn[8] = {R.s0[i].x, R.s0[i].y, R.s0[i].z, R.s0[i].w, R.s1[i].x, R.s1[i].y, R.s1[i].z, R.s1[i].w};
; #pragma unroll
;         for (int e = 0; e < 8; ++e) { o1[e] = fa[e] * cs[e] - fb[e] * sn[e]; o2[e] = fb[e] * cs[e] + fa[e] * sn[e]; }
;         *(LAS bf16x8*)(lds + LK + offb(row, pc)) = pack8(o1); *(LAS bf16x8*)(lds + LK + offb(row, pc + 8)) = pack8(o2);
;     }
; #pragma unroll
;     for (int i = 0; i < 4; ++i) { const int q4 = tid + 512 * i, row = q4 >> 4, ch = q4 & 15; *(LAS bf16x8*)(lds + LV + offb(row, ch)) = R.v[i]; }
; }
; __device__ __forceinline__ void unit(const bf16_t* __restrict__ proj, const float* __restrict__ rope, const float* __restrict__ log_decay, const float* __restrict__ gn_g, bf16_t* __restrict__ ymix, ...
;     ...
;         const int cq = 16 * w + r, tq = n * 128 + cq;
;         u32x2 qraw[2][4];
;         { const bf16_t* rp = proj + (size_t)(b * SEQ + tq) * DIN + OFF_QR + h * 128 + 4 * g;
; #pragma unroll
;           for (int ks = 0; ks < 2; ++ks) { qraw[ks][0] = *(const u32x2*)(rp + 32 * ks); qraw[ks][1] = *(const u32x2*)(rp + 32 * ks + 16); qraw[ks][2] = *(const u32x2*)(rp + 32 * ks + 64); qraw[ks][3] = *(const u32x2*)(rp + 32 * ks + 80); } }
;         __syncthreads();
;         kv_store(lds, raw, tid);
.LBB0_301:
	s_waitcnt vmcnt(0)
	v_lshlrev_b32_e32 v118, 16, v76
	v_and_b32_e32 v119, 0xffff0000, v76
	v_lshlrev_b32_e32 v120, 16, v72
	v_and_b32_e32 v121, 0xffff0000, v72
	v_pk_mul_f32 v[124:125], v[92:93], v[118:119]
	v_pk_mul_f32 v[92:93], v[92:93], v[120:121]
	v_lshlrev_b32_e32 v76, 16, v77
	v_and_b32_e32 v77, 0xffff0000, v77
	v_pk_fma_f32 v[124:125], v[88:89], v[120:121], v[124:125]
	v_pk_fma_f32 v[88:89], v[88:89], v[118:119], v[92:93] neg_lo:[0,0,1] neg_hi:[0,0,1]
	v_lshlrev_b32_e32 v72, 16, v73
	v_and_b32_e32 v73, 0xffff0000, v73
	v_pk_mul_f32 v[92:93], v[94:95], v[76:77]
	v_mov_b32_e32 v185, v201
	v_pk_fma_f32 v[92:93], v[90:91], v[72:73], v[92:93]
	v_pk_mul_f32 v[72:73], v[94:95], v[72:73]
	s_add_i32 s9, s2, s84
	v_pk_fma_f32 v[72:73], v[90:91], v[76:77], v[72:73] neg_lo:[0,0,1] neg_hi:[0,0,1]
	v_lshlrev_b32_e32 v76, 16, v78
	v_and_b32_e32 v77, 0xffff0000, v78
	v_lshlrev_b32_e32 v90, 16, v74
	v_and_b32_e32 v91, 0xffff0000, v74
	v_pk_mul_f32 v[94:95], v[84:85], v[76:77]
	v_pk_mul_f32 v[84:85], v[84:85], v[90:91]
	v_and_b32_e32 v117, 15, v185
	v_pk_fma_f32 v[94:95], v[80:81], v[90:91], v[94:95]
	v_pk_fma_f32 v[80:81], v[80:81], v[76:77], v[84:85] neg_lo:[0,0,1] neg_hi:[0,0,1]
	v_lshlrev_b32_e32 v76, 16, v79
	v_and_b32_e32 v77, 0xffff0000, v79
	v_add_u32_e32 v186, s9, v117
	v_mov_b64_e32 v[98:99], s[30:31]
	v_lshlrev_b32_e32 v122, 4, v185
	v_lshlrev_b32_e32 v74, 16, v75
	v_and_b32_e32 v75, 0xffff0000, v75
	v_pk_mul_f32 v[78:79], v[86:87], v[76:77]
	v_bfe_u32 v100, v185, 4, 2
	v_mad_i64_i32 v[96:97], s[86:87], v186, s67, v[98:99]
	v_and_b32_e32 v116, 0x70, v122
	v_pk_fma_f32 v[84:85], v[82:83], v[74:75], v[78:79]
	v_pk_mul_f32 v[74:75], v[86:87], v[74:75]
	s_add_i32 s39, 0, 0x24000
	v_lshl_add_u64 v[96:97], v[96:97], 0, v[180:181]
	v_lshlrev_b32_e32 v176, 3, v100
	v_add_u32_e32 v116, 0, v116
	v_pk_fma_f32 v[82:83], v[82:83], v[76:77], v[74:75] neg_lo:[0,0,1] neg_hi:[0,0,1]
	v_ashrrev_i32_e32 v74, 3, v185
	v_mov_b32_e32 v204, v203
	v_mov_b32_e32 v132, v202
	v_mov_b32_e32 v206, s39
	v_lshl_add_u64 v[96:97], v[96:97], 0, v[176:177]
	v_cvt_pk_bf16_f32 v76, v88, v89
	v_cvt_pk_bf16_f32 v77, v72, v73
	v_cvt_pk_bf16_f32 v78, v80, v81
	v_cvt_pk_bf16_f32 v79, v82, v83
	v_mad_u64_u32 v[72:73], s[86:87], v74, s68, v[116:117]
	v_lshlrev_b32_e32 v184, 2, v100
	global_load_dwordx2 v[108:109], v[96:97], off offset:3072
	global_load_dwordx2 v[110:111], v[96:97], off offset:3104
	global_load_dwordx2 v[114:115], v[96:97], off offset:3200
	global_load_dwordx2 v[112:113], v[96:97], off offset:3232
	global_load_dwordx2 v[104:105], v[96:97], off offset:3136
	global_load_dwordx2 v[100:101], v[96:97], off offset:3168
	global_load_dwordx2 v[106:107], v[96:97], off offset:3264
	global_load_dwordx2 v[102:103], v[96:97], off offset:3296
	s_waitcnt lgkmcnt(0)
	s_barrier
	ds_write_b128 v72, v[76:79]
	v_cvt_pk_bf16_f32 v76, v124, v125
	v_cvt_pk_bf16_f32 v77, v92, v93
	v_cvt_pk_bf16_f32 v78, v94, v95
	v_cvt_pk_bf16_f32 v79, v84, v85
	ds_write_b128 v72, v[76:79] offset:128
	v_lshlrev_b32_e32 v72, 16, v44
	v_and_b32_e32 v73, 0xffff0000, v44
	v_lshlrev_b32_e32 v76, 16, v40
	v_and_b32_e32 v77, 0xffff0000, v40
	v_pk_mul_f32 v[78:79], v[68:69], v[72:73]
	v_pk_mul_f32 v[68:69], v[68:69], v[76:77]
	v_lshlrev_b32_e32 v44, 16, v45
	v_and_b32_e32 v45, 0xffff0000, v45
	v_pk_fma_f32 v[78:79], v[64:65], v[76:77], v[78:79]
	v_pk_fma_f32 v[76:77], v[64:65], v[72:73], v[68:69] neg_lo:[0,0,1] neg_hi:[0,0,1]
	v_lshlrev_b32_e32 v40, 16, v41
	v_and_b32_e32 v41, 0xffff0000, v41
	v_pk_mul_f32 v[64:65], v[70:71], v[44:45]
	v_add_u32_e32 v75, 0x200, v185
	v_pk_fma_f32 v[80:81], v[66:67], v[40:41], v[64:65]
	v_pk_mul_f32 v[40:41], v[70:71], v[40:41]
	v_lshlrev_b32_e32 v64, 16, v42
	v_pk_fma_f32 v[40:41], v[66:67], v[44:45], v[40:41] neg_lo:[0,0,1] neg_hi:[0,0,1]
	v_lshlrev_b32_e32 v44, 16, v46
	v_and_b32_e32 v45, 0xffff0000, v46
	v_and_b32_e32 v65, 0xffff0000, v42
	v_pk_mul_f32 v[66:67], v[36:37], v[44:45]
	v_pk_mul_f32 v[36:37], v[36:37], v[64:65]
	v_add_lshl_u32 v46, s84, v117, 6
	v_pk_fma_f32 v[82:83], v[32:33], v[64:65], v[66:67]
	v_pk_fma_f32 v[36:37], v[32:33], v[44:45], v[36:37] neg_lo:[0,0,1] neg_hi:[0,0,1]
	v_lshlrev_b32_e32 v32, 16, v47
	v_and_b32_e32 v33, 0xffff0000, v47
	v_ashrrev_i32_e32 v47, 31, v46
	v_lshl_add_u64 v[46:47], v[46:47], 2, s[20:21]
	v_and_b32_e32 v64, 48, v185
	v_mov_b32_e32 v65, v177
	v_lshl_add_u64 v[46:47], v[46:47], 0, v[64:65]
	v_add_co_u32_e32 v72, vcc, s70, v46
	v_lshlrev_b32_e32 v42, 16, v43
	s_nop 0
	v_addc_co_u32_e32 v73, vcc, 0, v47, vcc
	global_load_dwordx4 v[68:71], v[72:73], off
	global_load_dwordx4 v[64:67], v[46:47], off
	v_and_b32_e32 v43, 0xffff0000, v43
	v_pk_mul_f32 v[44:45], v[38:39], v[32:33]
	v_pk_mul_f32 v[38:39], v[38:39], v[42:43]
	v_ashrrev_i32_e32 v188, 3, v75
	v_pk_fma_f32 v[38:39], v[34:35], v[32:33], v[38:39] neg_lo:[0,0,1] neg_hi:[0,0,1]
	v_pk_fma_f32 v[44:45], v[34:35], v[42:43], v[44:45]
	v_cvt_pk_bf16_f32 v32, v76, v77
	v_cvt_pk_bf16_f32 v33, v40, v41
	v_cvt_pk_bf16_f32 v34, v36, v37
	v_cvt_pk_bf16_f32 v35, v38, v39
	v_mad_u64_u32 v[36:37], s[86:87], v188, s68, v[116:117]
	ds_write_b128 v36, v[32:35]
	v_cvt_pk_bf16_f32 v32, v78, v79
	v_cvt_pk_bf16_f32 v33, v80, v81
	v_cvt_pk_bf16_f32 v34, v82, v83
	v_cvt_pk_bf16_f32 v35, v44, v45
	v_and_b32_e32 v172, 0xf0, v122
	ds_write_b128 v36, v[32:35] offset:128
	v_add_u32_e32 v32, 0, v172
	v_ashrrev_i32_e32 v173, 4, v185
	v_mad_u64_u32 v[34:35], s[86:87], v173, s68, v[32:33]
	v_ashrrev_i32_e32 v187, 4, v75
	ds_write_b128 v34, v[48:51] offset:36864
	v_mad_u64_u32 v[34:35], s[86:87], v187, s68, v[32:33]
	v_add_u32_e32 v33, 0x400, v185
	v_ashrrev_i32_e32 v174, 4, v33
; #define LAS __attribute__((address_space(3)))
; __device__ __forceinline__ unsigned cvtpk(float lo, float hi) { const f32x2 v = {lo, hi}; return __builtin_bit_cast(unsigned, __builtin_convertvector(v, bfx2)); }
; __device__ __forceinline__ bf16x8 pack8(const float (&f)[8]) { u32x4 u; u.x = cvtpk(f[0], f[1]); u.y = cvtpk(f[2], f[3]); u.z = cvtpk(f[4], f[5]); u.w = cvtpk(f[6], f[7]); return __builtin_bit_cast(bf16x8, u); }
; __device__ __forceinline__ void unit(const bf16_t* __restrict__ proj, const float* __restrict__ rope, const float* __restrict__ log_decay, const float* __restrict__ gn_g, bf16_t* __restrict__ ymix, ...
;     ...
; #pragma unroll
;         for (int nb = 0; nb < 8; ++nb) { u32x2 o; o.x = cvtpk(racc[nb][0], racc[nb][1]); o.y = cvtpk(racc[nb][2], racc[nb][3]);
;             *(LAS u32x2*)(lds + LRF + offb(16 * nb + r, 2 * w + (g >> 1)) + 8 * (g & 1)) = o; }
;         bf16x8 qn[4], qf[4], qb[4];
;         { const float sf = __builtin_amdgcn_exp2f((float)(cq + 1) * lf2), sb = __builtin_amdgcn_exp2f((float)(128 - cq) * lb2);
; #pragma unroll
;           for (int ks = 0; ks < 2; ++ks) {
;               float fa[8], fb[8], o1[8], o2[8], t1[8], t2[8];
;               { const u32x2 a0 = qraw[ks][0], a1 = qraw[ks][1], b0 = qraw[ks][2], b1 = qraw[ks][3];
;                 unpack8(__builtin_bit_cast(bf16x8, (u32x4){a0.x, a0.y, a1.x, a1.y}), fa); unpack8(__builtin_bit_cast(bf16x8, (u32x4){b0.x, b0.y, b1.x, b1.y}), fb); }
;               const float* cp = rope + tq * 64 + 32 * ks + 4 * g; const float* sp = cp + SEQ * 64;
;               const f32x4 c0 = *(const f32x4*)cp, c1 = *(const f32x4*)(cp + 16), s0 = *(const f32x4*)sp, s1 = *(const f32x4*)(sp + 16);
;               const float cs[8] = {c0.x, c0.y, c0.z, c0.w, c1.x, c1.y, c1.z, c1.w}, sn[8] = {s0.x, s0.y, s0.z, s0.w, s1.x, s1.y, s1.z, s1.w};
; #pragma unroll
;               for (int e = 0; e < 8; ++e) { o1[e] = fa[e] * cs[e] - fb[e] * sn[e]; o2[e] = fb[e] * cs[e] + fa[e] * sn[e]; }
;               qn[ks] = pack8(o1); qn[ks + 2] = pack8(o2);
; #pragma unroll
;               for (int e = 0; e < 8; ++e) { t1[e] = o1[e] * sf; t2[e] = o2[e] * sf; }
;               qf[ks] = pack8(t1); qf[ks + 2] = pack8(t2);
; #pragma unroll
;               for (int e = 0; e < 8; ++e) { t1[e] = o1[e] * sb; t2[e] = o2[e] * sb; }
;               qb[ks] = pack8(t1); qb[ks + 2] = pack8(t2);
;           } }
	ds_write_b128 v34, v[52:55] offset:36864
	v_mad_u64_u32 v[34:35], s[86:87], v174, s68, v[32:33]
	v_add_u32_e32 v33, 0x600, v185
	v_ashrrev_i32_e32 v175, 4, v33
	ds_write_b128 v34, v[60:63] offset:36864
	v_mad_u64_u32 v[32:33], s[86:87], v175, s68, v[32:33]
	global_load_dwordx4 v[42:45], v[72:73], off offset:64
	global_load_dwordx4 v[38:41], v[46:47], off offset:64
	ds_write_b128 v32, v[56:59] offset:36864
	v_lshrrev_b32_e32 v32, 1, v185
	v_or_b32_e32 v133, s3, v117
	v_and_b32_e32 v32, 16, v32
	v_add_u32_e32 v34, s4, v32
	v_and_b32_e32 v35, 8, v176
	v_mul_u32_u24_e32 v55, 0x120, v117
	v_add_u32_e32 v37, 1, v133
	v_cvt_pk_bf16_f32 v32, v20, v21
	v_cvt_pk_bf16_f32 v33, v22, v23
	v_add3_u32 v36, v34, v35, v55
	v_cvt_pk_bf16_f32 v34, v0, v1
	v_cvt_pk_bf16_f32 v35, v2, v3
	v_cvt_f32_i32_e32 v37, v37
	v_sub_u32_e32 v48, 0x80, v133
	ds_write2st64_b64 v36, v[32:33], v[34:35] offset1:9
	v_cvt_pk_bf16_f32 v32, v16, v17
	v_cvt_pk_bf16_f32 v33, v18, v19
	v_cvt_pk_bf16_f32 v34, v24, v25
	v_cvt_pk_bf16_f32 v35, v26, v27
	v_cvt_f32_i32_e32 v48, v48
	ds_write2st64_b64 v36, v[32:33], v[34:35] offset0:18 offset1:27
	v_cvt_pk_bf16_f32 v32, v4, v5
	v_cvt_pk_bf16_f32 v33, v6, v7
	v_cvt_pk_bf16_f32 v34, v8, v9
	v_cvt_pk_bf16_f32 v35, v10, v11
	ds_write2st64_b64 v36, v[32:33], v[34:35] offset0:36 offset1:45
	v_cvt_pk_bf16_f32 v32, v12, v13
	v_cvt_pk_bf16_f32 v33, v14, v15
	v_cvt_pk_bf16_f32 v34, v28, v29
	v_cvt_pk_bf16_f32 v35, v30, v31
	ds_write2st64_b64 v36, v[32:33], v[34:35] offset0:54 offset1:63
	v_mul_f32_e32 v32, v204, v37
	v_exp_f32_e32 v56, v32
	v_mul_f32_e32 v32, v132, v48
	v_exp_f32_e32 v54, v32
	s_waitcnt vmcnt(11)
	v_lshlrev_b32_e32 v34, 16, v108
	v_and_b32_e32 v35, 0xffff0000, v108
	global_load_dwordx4 v[76:79], v[72:73], off offset:128
	global_load_dwordx4 v[80:83], v[46:47], off offset:128
	s_waitcnt vmcnt(11)
	v_lshlrev_b32_e32 v36, 16, v114
	v_and_b32_e32 v37, 0xffff0000, v114
	s_waitcnt vmcnt(5)
	v_pk_mul_f32 v[32:33], v[68:69], v[34:35]
	v_bfe_u32 v123, v185, 2, 2
	s_waitcnt vmcnt(4)
	v_pk_fma_f32 v[48:49], v[64:65], v[36:37], v[32:33]
	v_pk_mul_f32 v[36:37], v[68:69], v[36:37]
	v_cvt_pk_bf16_f32 v32, v48, v49
	v_pk_fma_f32 v[34:35], v[64:65], v[34:35], v[36:37] neg_lo:[0,0,1] neg_hi:[0,0,1]
	v_pk_mul_f32 v[50:51], v[56:57], v[48:49] op_sel_hi:[0,1]
	v_pk_mul_f32 v[58:59], v[54:55], v[48:49] op_sel_hi:[0,1]
	v_cvt_pk_bf16_f32 v36, v34, v35
	v_pk_mul_f32 v[48:49], v[56:57], v[34:35] op_sel_hi:[0,1]
	v_pk_mul_f32 v[60:61], v[54:55], v[34:35] op_sel_hi:[0,1]
	v_lshlrev_b32_e32 v34, 16, v109
	v_and_b32_e32 v35, 0xffff0000, v109
	v_cvt_pk_bf16_f32 v108, v50, v51
	v_cvt_pk_bf16_f32 v116, v48, v49
	v_lshlrev_b32_e32 v48, 16, v115
	v_and_b32_e32 v49, 0xffff0000, v115
	v_pk_mul_f32 v[50:51], v[70:71], v[34:35]
	v_lshlrev_b32_e32 v68, 16, v112
	v_pk_fma_f32 v[50:51], v[66:67], v[48:49], v[50:51]
	v_pk_mul_f32 v[48:49], v[70:71], v[48:49]
	v_pk_mul_f32 v[52:53], v[56:57], v[50:51] op_sel_hi:[0,1]
	v_cvt_pk_bf16_f32 v33, v50, v51
	v_cvt_pk_bf16_f32 v109, v52, v53
	v_pk_mul_f32 v[62:63], v[54:55], v[50:51] op_sel_hi:[0,1]
	v_pk_fma_f32 v[34:35], v[66:67], v[34:35], v[48:49] neg_lo:[0,0,1] neg_hi:[0,0,1]
	global_load_dwordx4 v[50:53], v[72:73], off offset:192
	s_nop 0
	global_load_dwordx4 v[46:49], v[46:47], off offset:192
	v_pk_mul_f32 v[64:65], v[56:57], v[34:35] op_sel_hi:[0,1]
	v_lshlrev_b32_e32 v66, 16, v110
	v_and_b32_e32 v67, 0xffff0000, v110
	v_and_b32_e32 v69, 0xffff0000, v112
	v_cvt_pk_bf16_f32 v37, v34, v35
	v_cvt_pk_bf16_f32 v117, v64, v65
	v_pk_mul_f32 v[64:65], v[54:55], v[34:35] op_sel_hi:[0,1]
	v_cvt_pk_bf16_f32 v124, v58, v59
	v_cvt_pk_bf16_f32 v128, v60, v61
	v_cvt_pk_bf16_f32 v125, v62, v63
	s_waitcnt vmcnt(5)
	v_pk_mul_f32 v[34:35], v[42:43], v[66:67]
	v_pk_mul_f32 v[42:43], v[42:43], v[68:69]
	s_waitcnt vmcnt(4)
	v_pk_fma_f32 v[70:71], v[38:39], v[68:69], v[34:35]
	v_pk_fma_f32 v[42:43], v[38:39], v[66:67], v[42:43] neg_lo:[0,0,1] neg_hi:[0,0,1]
	v_pk_mul_f32 v[72:73], v[56:57], v[70:71] op_sel_hi:[0,1]
	v_pk_mul_f32 v[66:67], v[56:57], v[42:43] op_sel_hi:[0,1]
	v_cvt_pk_bf16_f32 v118, v66, v67
	v_lshlrev_b32_e32 v66, 16, v111
	v_and_b32_e32 v67, 0xffff0000, v111
	v_lshlrev_b32_e32 v68, 16, v113
	v_and_b32_e32 v69, 0xffff0000, v113
	v_cvt_pk_bf16_f32 v110, v72, v73
	v_pk_mul_f32 v[72:73], v[44:45], v[66:67]
	v_pk_mul_f32 v[44:45], v[44:45], v[68:69]
	v_cvt_pk_bf16_f32 v38, v42, v43
	v_pk_mul_f32 v[42:43], v[54:55], v[42:43] op_sel_hi:[0,1]
	v_pk_fma_f32 v[72:73], v[40:41], v[68:69], v[72:73]
	v_pk_fma_f32 v[40:41], v[40:41], v[66:67], v[44:45] neg_lo:[0,0,1] neg_hi:[0,0,1]
	v_cvt_pk_bf16_f32 v130, v42, v43
	v_cvt_pk_bf16_f32 v39, v40, v41
	v_pk_mul_f32 v[44:45], v[56:57], v[40:41] op_sel_hi:[0,1]
	v_pk_mul_f32 v[40:41], v[54:55], v[40:41] op_sel_hi:[0,1]
	v_lshlrev_b32_e32 v42, 16, v104
	v_and_b32_e32 v43, 0xffff0000, v104
	v_cvt_pk_bf16_f32 v119, v44, v45
	v_cvt_pk_bf16_f32 v131, v40, v41
	v_lshlrev_b32_e32 v44, 16, v106
	v_and_b32_e32 v45, 0xffff0000, v106
	v_cvt_pk_bf16_f32 v129, v64, v65
	v_lshlrev_b32_e32 v64, 16, v107
	v_and_b32_e32 v65, 0xffff0000, v107
	v_cvt_pk_bf16_f32 v34, v70, v71
	v_pk_mul_f32 v[70:71], v[54:55], v[70:71] op_sel_hi:[0,1]
	v_lshlrev_b32_e32 v68, 16, v100
	v_and_b32_e32 v69, 0xffff0000, v100
	v_cvt_pk_bf16_f32 v126, v70, v71
	v_lshlrev_b32_e32 v70, 16, v102
	v_and_b32_e32 v71, 0xffff0000, v102
	v_cvt_pk_bf16_f32 v35, v72, v73
	s_waitcnt vmcnt(3)
	v_pk_mul_f32 v[40:41], v[76:77], v[42:43]
	v_pk_mul_f32 v[84:85], v[56:57], v[72:73] op_sel_hi:[0,1]
	s_waitcnt vmcnt(2)
; #define LAS __attribute__((address_space(3)))
; __device__ __forceinline__ bf16x8 pack8(const float (&f)[8]) { u32x4 u; u.x = cvtpk(f[0], f[1]); u.y = cvtpk(f[2], f[3]); u.z = cvtpk(f[4], f[5]); u.w = cvtpk(f[6], f[7]); return __builtin_bit_cast(bf16x8, u); }
; __device__ __forceinline__ void unit(const bf16_t* __restrict__ proj, const float* __restrict__ rope, const float* __restrict__ log_decay, const float* __restrict__ gn_g, bf16_t* __restrict__ ymix, ...
;     ...
;         for (int ks2 = 0; ks2 < 4; ++ks2) {
;             float pv[8];
; #pragma unroll
;             for (int hb = 0; hb < 2; ++hb) {
;                 const int mb = 2 * ks2 + hb;
;                 f32x4 st = (f32x4){0.f, 0.f, 0.f, 0.f};
; #pragma unroll
;                 for (int ks = 0; ks < 4; ++ks) { const LAS unsigned char* kp = lds + LK + zo3 + RS * (16 * mb + r) + 64 * ks + 8 * g; const u32x2 k0 = *(const LAS u32x2*)kp, k1 = *(const LAS u32x2*)(kp + 32);
;                     st = __builtin_amdgcn_mfma_f32_16x16x32_bf16(__builtin_bit_cast(bf16x8, (u32x4){k0.x, k0.y, k1.x, k1.y}), qn[ks], st, 0, 0, 0); }
; #pragma unroll
;                 for (int j = 0; j < 4; ++j) { const int diff = cq - (16 * mb + 4 * g + j); pv[4 * hb + j] = st[j] * __builtin_amdgcn_exp2f(diff >= 0 ? (float)diff * lf2 : (float)(-diff) * lb2); }
;             }
;             pt[ks2] = pack8(pv);
;         }
	v_pk_fma_f32 v[58:59], v[80:81], v[44:45], v[40:41]
	v_pk_mul_f32 v[44:45], v[76:77], v[44:45]
	v_pk_mul_f32 v[60:61], v[56:57], v[58:59] op_sel_hi:[0,1]
	v_pk_fma_f32 v[42:43], v[80:81], v[42:43], v[44:45] neg_lo:[0,0,1] neg_hi:[0,0,1]
	v_cvt_pk_bf16_f32 v120, v60, v61
	v_cvt_pk_bf16_f32 v44, v42, v43
	v_pk_mul_f32 v[60:61], v[56:57], v[42:43] op_sel_hi:[0,1]
	v_pk_mul_f32 v[62:63], v[54:55], v[42:43] op_sel_hi:[0,1]
	v_lshlrev_b32_e32 v42, 16, v105
	v_and_b32_e32 v43, 0xffff0000, v105
	v_cvt_pk_bf16_f32 v136, v60, v61
	v_pk_mul_f32 v[60:61], v[78:79], v[42:43]
	v_pk_mul_f32 v[72:73], v[54:55], v[72:73] op_sel_hi:[0,1]
	v_pk_fma_f32 v[60:61], v[82:83], v[64:65], v[60:61]
	v_pk_mul_f32 v[64:65], v[78:79], v[64:65]
	v_pk_mul_f32 v[66:67], v[56:57], v[60:61] op_sel_hi:[0,1]
	v_pk_fma_f32 v[42:43], v[82:83], v[42:43], v[64:65] neg_lo:[0,0,1] neg_hi:[0,0,1]
	v_cvt_pk_bf16_f32 v121, v66, v67
	v_cvt_pk_bf16_f32 v45, v42, v43
	v_pk_mul_f32 v[64:65], v[56:57], v[42:43] op_sel_hi:[0,1]
	v_pk_mul_f32 v[66:67], v[54:55], v[42:43] op_sel_hi:[0,1]
	v_cvt_pk_bf16_f32 v137, v64, v65
	v_cvt_pk_bf16_f32 v127, v72, v73
	v_cvt_pk_bf16_f32 v40, v58, v59
	v_pk_mul_f32 v[58:59], v[54:55], v[58:59] op_sel_hi:[0,1]
	v_cvt_pk_bf16_f32 v41, v60, v61
	v_pk_mul_f32 v[60:61], v[54:55], v[60:61] op_sel_hi:[0,1]
	s_waitcnt vmcnt(1)
	v_pk_mul_f32 v[42:43], v[50:51], v[68:69]
	v_pk_mul_f32 v[50:51], v[50:51], v[70:71]
	s_waitcnt vmcnt(0)
	v_pk_fma_f32 v[64:65], v[46:47], v[70:71], v[42:43]
	v_pk_fma_f32 v[50:51], v[46:47], v[68:69], v[50:51] neg_lo:[0,0,1] neg_hi:[0,0,1]
	v_pk_mul_f32 v[72:73], v[56:57], v[64:65] op_sel_hi:[0,1]
	v_cvt_pk_bf16_f32 v122, v72, v73
	v_pk_mul_f32 v[68:69], v[56:57], v[50:51] op_sel_hi:[0,1]
	v_lshlrev_b32_e32 v70, 16, v101
	v_and_b32_e32 v71, 0xffff0000, v101
	v_lshlrev_b32_e32 v72, 16, v103
	v_and_b32_e32 v73, 0xffff0000, v103
	v_cvt_pk_bf16_f32 v138, v68, v69
	v_pk_mul_f32 v[68:69], v[52:53], v[70:71]
	v_pk_mul_f32 v[52:53], v[52:53], v[72:73]
	v_pk_fma_f32 v[68:69], v[48:49], v[72:73], v[68:69]
	v_pk_fma_f32 v[48:49], v[48:49], v[70:71], v[52:53] neg_lo:[0,0,1] neg_hi:[0,0,1]
	v_cvt_pk_bf16_f32 v42, v64, v65
	v_pk_mul_f32 v[64:65], v[54:55], v[64:65] op_sel_hi:[0,1]
	v_cvt_pk_bf16_f32 v46, v50, v51
	v_pk_mul_f32 v[50:51], v[54:55], v[50:51] op_sel_hi:[0,1]
	v_add3_u32 v55, 0, v176, v55
	v_pk_mul_f32 v[52:53], v[56:57], v[48:49] op_sel_hi:[0,1]
	s_waitcnt vmcnt(0)
	s_waitcnt lgkmcnt(0)
	s_barrier
	ds_read2_b64 v[76:79], v55 offset1:4
	v_cvt_pk_bf16_f32 v139, v52, v53
	v_sub_u32_e32 v53, v133, v184
	v_sub_u32_e32 v57, 0, v53
	v_max_i32_e32 v57, v53, v57
	v_cvt_f32_u32_e32 v57, v57
	ds_read2_b64 v[70:73], v55 offset0:8 offset1:12
	v_cmp_gt_i32_e32 vcc, 0, v53
	s_waitcnt lgkmcnt(1)
	v_mfma_f32_16x16x32_bf16 v[76:79], v[76:79], v[36:39], 0
	v_cndmask_b32_e32 v53, v204, v132, vcc
	v_mul_f32_e32 v53, v53, v57
	v_xad_u32 v57, v184, -1, v133
	v_sub_u32_e32 v75, 0, v57
	ds_read2_b64 v[80:83], v55 offset0:16 offset1:20
	v_max_i32_e32 v75, v57, v75
	v_cvt_f32_u32_e32 v75, v75
	v_cvt_pk_bf16_f32 v47, v48, v49
	v_cmp_gt_i32_e32 vcc, 0, v57
	v_or_b32_e32 v57, 2, v184
	s_waitcnt lgkmcnt(1)
	v_mfma_f32_16x16x32_bf16 v[70:73], v[70:73], v[44:47], v[76:79]
	v_exp_f32_e32 v88, v53
	v_cndmask_b32_e32 v53, v204, v132, vcc
	v_sub_u32_e32 v57, v133, v57
	ds_read2_b64 v[76:79], v55 offset0:24 offset1:28
	v_mul_f32_e32 v53, v53, v75
	v_sub_u32_e32 v75, 0, v57
	v_max_i32_e32 v75, v57, v75
	v_cvt_f32_u32_e32 v75, v75
	s_waitcnt lgkmcnt(1)
	v_mfma_f32_16x16x32_bf16 v[70:73], v[80:83], v[32:35], v[70:73]
	v_cmp_gt_i32_e32 vcc, 0, v57
	v_exp_f32_e32 v89, v53
	v_cvt_pk_bf16_f32 v43, v68, v69
	v_cndmask_b32_e32 v53, v204, v132, vcc
	v_mul_f32_e32 v53, v53, v75
	v_exp_f32_e32 v90, v53
	v_add_u32_e32 v53, 0x1000, v55
	s_waitcnt lgkmcnt(0)
	v_mfma_f32_16x16x32_bf16 v[70:73], v[76:79], v[40:43], v[70:73]
	ds_read2_b64 v[76:79], v53 offset0:64 offset1:68
	ds_read2_b64 v[80:83], v53 offset0:72 offset1:76
	v_or_b32_e32 v57, 3, v184
	v_sub_u32_e32 v57, v133, v57
	v_sub_u32_e32 v75, 0, v57
	v_max_i32_e32 v75, v57, v75
	s_waitcnt lgkmcnt(1)
	v_mfma_f32_16x16x32_bf16 v[76:79], v[76:79], v[36:39], 0
	v_cmp_gt_i32_e32 vcc, 0, v57
	v_cvt_f32_u32_e32 v57, v75
	v_cvt_pk_bf16_f32 v111, v84, v85
	ds_read2_b64 v[84:87], v53 offset0:80 offset1:84
	v_cndmask_b32_e32 v75, v204, v132, vcc
	s_waitcnt lgkmcnt(1)
	v_mfma_f32_16x16x32_bf16 v[76:79], v[80:83], v[44:47], v[76:79]
	ds_read2_b64 v[80:83], v53 offset0:88 offset1:92
	v_or_b32_e32 v53, 16, v184
	v_mul_f32_e32 v57, v75, v57
	v_sub_u32_e32 v53, v133, v53
	v_exp_f32_e32 v91, v57
	v_sub_u32_e32 v57, 0, v53
	v_max_i32_e32 v57, v53, v57
	v_cvt_f32_u32_e32 v57, v57
	v_cmp_gt_i32_e32 vcc, 0, v53
	v_pk_mul_f32 v[88:89], v[88:89], v[70:71]
	v_pk_mul_f32 v[90:91], v[90:91], v[72:73]
	v_cndmask_b32_e32 v53, v204, v132, vcc
	v_mul_f32_e32 v53, v53, v57
	v_or_b32_e32 v57, 17, v184
	v_sub_u32_e32 v57, v133, v57
	v_sub_u32_e32 v75, 0, v57
	v_max_i32_e32 v75, v57, v75
	v_cvt_f32_u32_e32 v75, v75
	v_cmp_gt_i32_e32 vcc, 0, v57
	v_or_b32_e32 v57, 18, v184
	s_waitcnt lgkmcnt(1)
	v_mfma_f32_16x16x32_bf16 v[70:73], v[84:87], v[32:35], v[76:79]
	v_exp_f32_e32 v84, v53
	v_cndmask_b32_e32 v53, v204, v132, vcc
	v_sub_u32_e32 v57, v133, v57
	v_mul_f32_e32 v53, v53, v75
	v_sub_u32_e32 v75, 0, v57
	v_max_i32_e32 v75, v57, v75
	v_cvt_f32_u32_e32 v75, v75
	v_cmp_gt_i32_e32 vcc, 0, v57
	v_exp_f32_e32 v85, v53
	s_waitcnt lgkmcnt(0)
; #define LAS __attribute__((address_space(3)))
; __device__ __forceinline__ bf16x8 pack8(const float (&f)[8]) { u32x4 u; u.x = cvtpk(f[0], f[1]); u.y = cvtpk(f[2], f[3]); u.z = cvtpk(f[4], f[5]); u.w = cvtpk(f[6], f[7]); return __builtin_bit_cast(bf16x8, u); }
; __device__ __forceinline__ void unit(const bf16_t* __restrict__ proj, const float* __restrict__ rope, const float* __restrict__ log_decay, const float* __restrict__ gn_g, bf16_t* __restrict__ ymix, ...
;     ...
;         for (int ks2 = 0; ks2 < 4; ++ks2) {
;             float pv[8];
; #pragma unroll
;             for (int hb = 0; hb < 2; ++hb) {
;                 const int mb = 2 * ks2 + hb;
;                 f32x4 st = (f32x4){0.f, 0.f, 0.f, 0.f};
; #pragma unroll
;                 for (int ks = 0; ks < 4; ++ks) { const LAS unsigned char* kp = lds + LK + zo3 + RS * (16 * mb + r) + 64 * ks + 8 * g; const u32x2 k0 = *(const LAS u32x2*)kp, k1 = *(const LAS u32x2*)(kp + 32);
;                     st = __builtin_amdgcn_mfma_f32_16x16x32_bf16(__builtin_bit_cast(bf16x8, (u32x4){k0.x, k0.y, k1.x, k1.y}), qn[ks], st, 0, 0, 0); }
; #pragma unroll
;                 for (int j = 0; j < 4; ++j) { const int diff = cq - (16 * mb + 4 * g + j); pv[4 * hb + j] = st[j] * __builtin_amdgcn_exp2f(diff >= 0 ? (float)diff * lf2 : (float)(-diff) * lb2); }
;             }
;             pt[ks2] = pack8(pv);
;         }
	v_mfma_f32_16x16x32_bf16 v[70:73], v[80:83], v[40:43], v[70:73]
	v_cndmask_b32_e32 v53, v204, v132, vcc
	v_mul_f32_e32 v53, v53, v75
	v_exp_f32_e32 v92, v53
	v_or_b32_e32 v53, 19, v184
	v_sub_u32_e32 v53, v133, v53
	v_sub_u32_e32 v57, 0, v53
	v_max_i32_e32 v57, v53, v57
	v_cvt_f32_u32_e32 v57, v57
	v_add_u32_e32 v75, 0x2000, v55
	ds_read2_b64 v[76:79], v75 offset0:128 offset1:132
	v_cmp_gt_i32_e32 vcc, 0, v53
	ds_read2_b64 v[80:83], v75 offset0:136 offset1:140
	s_waitcnt lgkmcnt(1)
	v_mfma_f32_16x16x32_bf16 v[76:79], v[76:79], v[36:39], 0
	v_cndmask_b32_e32 v53, v204, v132, vcc
	v_mul_f32_e32 v53, v53, v57
	v_exp_f32_e32 v93, v53
	v_or_b32_e32 v53, 32, v184
	v_sub_u32_e32 v53, v133, v53
	v_sub_u32_e32 v57, 0, v53
	v_max_i32_e32 v57, v53, v57
	v_cvt_f32_u32_e32 v57, v57
	v_cmp_gt_i32_e32 vcc, 0, v53
	v_pk_mul_f32 v[94:95], v[84:85], v[70:71]
	ds_read2_b64 v[84:87], v75 offset0:144 offset1:148
	v_cndmask_b32_e32 v53, v204, v132, vcc
	v_mul_f32_e32 v53, v53, v57
	v_or_b32_e32 v57, 33, v184
	v_sub_u32_e32 v57, v133, v57
	v_pk_mul_f32 v[92:93], v[92:93], v[72:73]
	s_waitcnt lgkmcnt(1)
	v_mfma_f32_16x16x32_bf16 v[70:73], v[80:83], v[44:47], v[76:79]
	v_cmp_gt_i32_e32 vcc, 0, v57
	v_cvt_pk_bf16_f32 v156, v88, v89
	v_exp_f32_e32 v88, v53
	ds_read2_b64 v[76:79], v75 offset0:152 offset1:156
	v_sub_u32_e32 v75, 0, v57
	v_max_i32_e32 v75, v57, v75
	v_cvt_f32_u32_e32 v75, v75
	v_or_b32_e32 v57, 34, v184
	v_cndmask_b32_e32 v53, v204, v132, vcc
	v_sub_u32_e32 v57, v133, v57
	v_mul_f32_e32 v53, v53, v75
	v_sub_u32_e32 v75, 0, v57
	v_max_i32_e32 v75, v57, v75
	v_cvt_f32_u32_e32 v75, v75
	s_waitcnt lgkmcnt(1)
	v_mfma_f32_16x16x32_bf16 v[70:73], v[84:87], v[32:35], v[70:73]
	v_cmp_gt_i32_e32 vcc, 0, v57
	v_exp_f32_e32 v89, v53
	v_cvt_pk_bf16_f32 v157, v90, v91
	v_cndmask_b32_e32 v53, v204, v132, vcc
	v_mul_f32_e32 v53, v53, v75
	v_exp_f32_e32 v90, v53
	v_add_u32_e32 v53, 0x3000, v55
	s_waitcnt lgkmcnt(0)
	v_mfma_f32_16x16x32_bf16 v[70:73], v[76:79], v[40:43], v[70:73]
	ds_read2_b64 v[76:79], v53 offset0:192 offset1:196
	ds_read2_b64 v[80:83], v53 offset0:200 offset1:204
	v_or_b32_e32 v57, 35, v184
	v_sub_u32_e32 v57, v133, v57
	v_sub_u32_e32 v75, 0, v57
	v_max_i32_e32 v75, v57, v75
	s_waitcnt lgkmcnt(1)
	v_mfma_f32_16x16x32_bf16 v[76:79], v[76:79], v[36:39], 0
	v_cmp_gt_i32_e32 vcc, 0, v57
	v_cvt_f32_u32_e32 v57, v75
	ds_read2_b64 v[84:87], v53 offset0:208 offset1:212
	v_cndmask_b32_e32 v75, v204, v132, vcc
	s_waitcnt lgkmcnt(1)
	v_mfma_f32_16x16x32_bf16 v[76:79], v[80:83], v[44:47], v[76:79]
	ds_read2_b64 v[80:83], v53 offset0:216 offset1:220
	v_or_b32_e32 v53, 48, v184
	v_mul_f32_e32 v57, v75, v57
	v_sub_u32_e32 v53, v133, v53
	v_exp_f32_e32 v91, v57
	v_sub_u32_e32 v57, 0, v53
	v_max_i32_e32 v57, v53, v57
	v_cvt_f32_u32_e32 v57, v57
	v_cmp_gt_i32_e32 vcc, 0, v53
	v_pk_mul_f32 v[88:89], v[88:89], v[70:71]
	v_pk_mul_f32 v[90:91], v[90:91], v[72:73]
	v_cndmask_b32_e32 v53, v204, v132, vcc
	v_mul_f32_e32 v53, v53, v57
	v_or_b32_e32 v57, 49, v184
	v_sub_u32_e32 v57, v133, v57
	v_sub_u32_e32 v75, 0, v57
	v_max_i32_e32 v75, v57, v75
	v_cvt_f32_u32_e32 v75, v75
	v_cmp_gt_i32_e32 vcc, 0, v57
	v_or_b32_e32 v57, 50, v184
	s_waitcnt lgkmcnt(1)
	v_mfma_f32_16x16x32_bf16 v[70:73], v[84:87], v[32:35], v[76:79]
	v_exp_f32_e32 v84, v53
	v_cndmask_b32_e32 v53, v204, v132, vcc
	v_sub_u32_e32 v57, v133, v57
	v_mul_f32_e32 v53, v53, v75
	v_sub_u32_e32 v75, 0, v57
	v_max_i32_e32 v75, v57, v75
	v_cvt_f32_u32_e32 v75, v75
	v_cmp_gt_i32_e32 vcc, 0, v57
	v_exp_f32_e32 v85, v53
	v_cvt_pk_bf16_f32 v159, v92, v93
	v_cndmask_b32_e32 v53, v204, v132, vcc
	v_mul_f32_e32 v53, v53, v75
	v_exp_f32_e32 v92, v53
	v_or_b32_e32 v53, 51, v184
	v_sub_u32_e32 v53, v133, v53
	v_sub_u32_e32 v57, 0, v53
	v_max_i32_e32 v57, v53, v57
	v_cvt_f32_u32_e32 v57, v57
	v_add_u32_e32 v75, 0x4800, v55
	ds_read2_b64 v[76:79], v75 offset1:4
	v_cmp_gt_i32_e32 vcc, 0, v53
	s_waitcnt lgkmcnt(1)
	v_mfma_f32_16x16x32_bf16 v[70:73], v[80:83], v[40:43], v[70:73]
	ds_read2_b64 v[80:83], v75 offset0:8 offset1:12
	v_cndmask_b32_e32 v53, v204, v132, vcc
	v_mul_f32_e32 v53, v53, v57
	v_exp_f32_e32 v93, v53
	v_or_b32_e32 v53, 64, v184
	v_sub_u32_e32 v53, v133, v53
	v_sub_u32_e32 v57, 0, v53
	v_max_i32_e32 v57, v53, v57
	v_cvt_f32_u32_e32 v57, v57
	s_waitcnt lgkmcnt(1)
	v_mfma_f32_16x16x32_bf16 v[76:79], v[76:79], v[36:39], 0
	v_cmp_gt_i32_e32 vcc, 0, v53
	v_cvt_pk_bf16_f32 v158, v94, v95
	v_pk_mul_f32 v[94:95], v[84:85], v[70:71]
	v_cndmask_b32_e32 v53, v204, v132, vcc
	v_mul_f32_e32 v53, v53, v57
	v_or_b32_e32 v57, 0x41, v184
	v_sub_u32_e32 v57, v133, v57
	ds_read2_b64 v[84:87], v75 offset0:16 offset1:20
	v_pk_mul_f32 v[92:93], v[92:93], v[72:73]
	s_waitcnt lgkmcnt(1)
	v_mfma_f32_16x16x32_bf16 v[70:73], v[80:83], v[44:47], v[76:79]
	v_cmp_gt_i32_e32 vcc, 0, v57
	v_cvt_pk_bf16_f32 v168, v88, v89
	v_exp_f32_e32 v88, v53
	ds_read2_b64 v[76:79], v75 offset0:24 offset1:28
	v_sub_u32_e32 v75, 0, v57
	v_max_i32_e32 v75, v57, v75
	v_cvt_f32_u32_e32 v75, v75
	v_or_b32_e32 v57, 0x42, v184
	v_cndmask_b32_e32 v53, v204, v132, vcc
	v_sub_u32_e32 v57, v133, v57
	v_mul_f32_e32 v53, v53, v75
	v_sub_u32_e32 v75, 0, v57
	v_max_i32_e32 v75, v57, v75
	v_cvt_f32_u32_e32 v75, v75
	s_waitcnt lgkmcnt(1)
	v_mfma_f32_16x16x32_bf16 v[70:73], v[84:87], v[32:35], v[70:73]
	v_cmp_gt_i32_e32 vcc, 0, v57
	v_exp_f32_e32 v89, v53
	v_cvt_pk_bf16_f32 v169, v90, v91
	v_cndmask_b32_e32 v53, v204, v132, vcc
	v_mul_f32_e32 v53, v53, v75
	v_exp_f32_e32 v90, v53
	v_add_u32_e32 v53, 0x5800, v55
	s_waitcnt lgkmcnt(0)
; #define LAS __attribute__((address_space(3)))
; __device__ __forceinline__ bf16x8 pack8(const float (&f)[8]) { u32x4 u; u.x = cvtpk(f[0], f[1]); u.y = cvtpk(f[2], f[3]); u.z = cvtpk(f[4], f[5]); u.w = cvtpk(f[6], f[7]); return __builtin_bit_cast(bf16x8, u); }
; __device__ __forceinline__ void unit(const bf16_t* __restrict__ proj, const float* __restrict__ rope, const float* __restrict__ log_decay, const float* __restrict__ gn_g, bf16_t* __restrict__ ymix, ...
;     ...
;         for (int ks2 = 0; ks2 < 4; ++ks2) {
;             float pv[8];
; #pragma unroll
;             for (int hb = 0; hb < 2; ++hb) {
;                 const int mb = 2 * ks2 + hb;
;                 f32x4 st = (f32x4){0.f, 0.f, 0.f, 0.f};
; #pragma unroll
;                 for (int ks = 0; ks < 4; ++ks) { const LAS unsigned char* kp = lds + LK + zo3 + RS * (16 * mb + r) + 64 * ks + 8 * g; const u32x2 k0 = *(const LAS u32x2*)kp, k1 = *(const LAS u32x2*)(kp + 32);
;                     st = __builtin_amdgcn_mfma_f32_16x16x32_bf16(__builtin_bit_cast(bf16x8, (u32x4){k0.x, k0.y, k1.x, k1.y}), qn[ks], st, 0, 0, 0); }
; #pragma unroll
;                 for (int j = 0; j < 4; ++j) { const int diff = cq - (16 * mb + 4 * g + j); pv[4 * hb + j] = st[j] * __builtin_amdgcn_exp2f(diff >= 0 ? (float)diff * lf2 : (float)(-diff) * lb2); }
;             }
;             pt[ks2] = pack8(pv);
;         }
	v_mfma_f32_16x16x32_bf16 v[70:73], v[76:79], v[40:43], v[70:73]
	ds_read2_b64 v[76:79], v53 offset0:64 offset1:68
	ds_read2_b64 v[80:83], v53 offset0:72 offset1:76
	v_or_b32_e32 v57, 0x43, v184
	v_sub_u32_e32 v57, v133, v57
	v_sub_u32_e32 v75, 0, v57
	v_max_i32_e32 v75, v57, v75
	s_waitcnt lgkmcnt(1)
	v_mfma_f32_16x16x32_bf16 v[76:79], v[76:79], v[36:39], 0
	v_cmp_gt_i32_e32 vcc, 0, v57
	v_cvt_f32_u32_e32 v57, v75
	ds_read2_b64 v[84:87], v53 offset0:80 offset1:84
	v_cndmask_b32_e32 v75, v204, v132, vcc
	s_waitcnt lgkmcnt(1)
	v_mfma_f32_16x16x32_bf16 v[76:79], v[80:83], v[44:47], v[76:79]
	ds_read2_b64 v[80:83], v53 offset0:88 offset1:92
	v_or_b32_e32 v53, 0x50, v184
	v_mul_f32_e32 v57, v75, v57
	v_sub_u32_e32 v53, v133, v53
	v_exp_f32_e32 v91, v57
	v_sub_u32_e32 v57, 0, v53
	v_max_i32_e32 v57, v53, v57
	v_cvt_f32_u32_e32 v57, v57
	v_cmp_gt_i32_e32 vcc, 0, v53
	v_cvt_pk_bf16_f32 v171, v92, v93
	v_cvt_pk_bf16_f32 v170, v94, v95
	v_cndmask_b32_e32 v53, v204, v132, vcc
	v_mul_f32_e32 v53, v53, v57
	v_or_b32_e32 v57, 0x51, v184
	v_sub_u32_e32 v57, v133, v57
	v_sub_u32_e32 v75, 0, v57
	v_max_i32_e32 v75, v57, v75
	v_cvt_f32_u32_e32 v75, v75
	v_cmp_gt_i32_e32 vcc, 0, v57
	v_or_b32_e32 v57, 0x52, v184
	v_exp_f32_e32 v92, v53
	v_cndmask_b32_e32 v53, v204, v132, vcc
	v_sub_u32_e32 v57, v133, v57
	v_mul_f32_e32 v53, v53, v75
	v_sub_u32_e32 v75, 0, v57
	v_max_i32_e32 v75, v57, v75
	v_cvt_f32_u32_e32 v75, v75
	v_cmp_gt_i32_e32 vcc, 0, v57
	v_exp_f32_e32 v93, v53
	v_pk_mul_f32 v[88:89], v[88:89], v[70:71]
	v_cndmask_b32_e32 v53, v204, v132, vcc
	v_mul_f32_e32 v53, v53, v75
	v_exp_f32_e32 v94, v53
	v_or_b32_e32 v53, 0x53, v184
	v_sub_u32_e32 v53, v133, v53
	v_sub_u32_e32 v57, 0, v53
	v_max_i32_e32 v57, v53, v57
	v_cvt_f32_u32_e32 v57, v57
	v_add_u32_e32 v75, 0x6800, v55
	v_pk_mul_f32 v[90:91], v[90:91], v[72:73]
	s_waitcnt lgkmcnt(1)
	v_mfma_f32_16x16x32_bf16 v[70:73], v[84:87], v[32:35], v[76:79]
	v_cmp_gt_i32_e32 vcc, 0, v53
	ds_read2_b64 v[84:87], v75 offset0:144 offset1:148
	v_cvt_pk_bf16_f32 v152, v88, v89
	ds_read2_b64 v[76:79], v75 offset0:128 offset1:132
	v_cndmask_b32_e32 v53, v204, v132, vcc
	v_mul_f32_e32 v53, v53, v57
	v_exp_f32_e32 v95, v53
	v_or_b32_e32 v53, 0x60, v184
	s_waitcnt lgkmcnt(2)
	v_mfma_f32_16x16x32_bf16 v[70:73], v[80:83], v[40:43], v[70:73]
	ds_read2_b64 v[80:83], v75 offset0:136 offset1:140
	v_sub_u32_e32 v53, v133, v53
	v_sub_u32_e32 v57, 0, v53
	v_max_i32_e32 v57, v53, v57
	v_cvt_f32_u32_e32 v57, v57
	s_waitcnt lgkmcnt(1)
	v_mfma_f32_16x16x32_bf16 v[76:79], v[76:79], v[36:39], 0
	v_cmp_gt_i32_e32 vcc, 0, v53
	v_pk_mul_f32 v[92:93], v[92:93], v[70:71]
	v_pk_mul_f32 v[94:95], v[94:95], v[72:73]
	v_cndmask_b32_e32 v53, v204, v132, vcc
	v_mul_f32_e32 v53, v53, v57
	v_or_b32_e32 v57, 0x61, v184
	v_sub_u32_e32 v57, v133, v57
	s_waitcnt lgkmcnt(0)
	v_mfma_f32_16x16x32_bf16 v[70:73], v[80:83], v[44:47], v[76:79]
	v_cmp_gt_i32_e32 vcc, 0, v57
	v_exp_f32_e32 v88, v53
	v_cvt_pk_bf16_f32 v153, v90, v91
	ds_read2_b64 v[76:79], v75 offset0:152 offset1:156
	v_sub_u32_e32 v75, 0, v57
	v_max_i32_e32 v75, v57, v75
	v_cvt_f32_u32_e32 v75, v75
	v_or_b32_e32 v57, 0x62, v184
	v_cndmask_b32_e32 v53, v204, v132, vcc
	v_sub_u32_e32 v57, v133, v57
	v_mul_f32_e32 v53, v53, v75
	v_sub_u32_e32 v75, 0, v57
	v_max_i32_e32 v75, v57, v75
	v_cvt_f32_u32_e32 v75, v75
	v_mfma_f32_16x16x32_bf16 v[70:73], v[84:87], v[32:35], v[70:73]
	v_cmp_gt_i32_e32 vcc, 0, v57
	v_exp_f32_e32 v89, v53
	v_pk_mul_f32 v[48:49], v[54:55], v[48:49] op_sel_hi:[0,1]
	v_cndmask_b32_e32 v53, v204, v132, vcc
	v_mul_f32_e32 v53, v53, v75
	v_exp_f32_e32 v90, v53
	v_add_u32_e32 v53, 0x7800, v55
	s_waitcnt lgkmcnt(0)
	v_mfma_f32_16x16x32_bf16 v[70:73], v[76:79], v[40:43], v[70:73]
	ds_read2_b64 v[76:79], v53 offset0:192 offset1:196
	ds_read2_b64 v[80:83], v53 offset0:200 offset1:204
	ds_read2_b64 v[84:87], v53 offset0:208 offset1:212
	v_or_b32_e32 v55, 0x63, v184
	s_waitcnt lgkmcnt(2)
	v_mfma_f32_16x16x32_bf16 v[36:39], v[76:79], v[36:39], 0
	v_sub_u32_e32 v55, v133, v55
	v_sub_u32_e32 v57, 0, v55
	v_max_i32_e32 v57, v55, v57
	v_cmp_gt_i32_e32 vcc, 0, v55
	v_cvt_f32_u32_e32 v55, v57
	s_waitcnt lgkmcnt(1)
	v_mfma_f32_16x16x32_bf16 v[36:39], v[80:83], v[44:47], v[36:39]
	v_cndmask_b32_e32 v57, v204, v132, vcc
	v_pk_mul_f32 v[44:45], v[88:89], v[70:71]
	v_mul_f32_e32 v55, v57, v55
	s_waitcnt lgkmcnt(0)
	v_mfma_f32_16x16x32_bf16 v[32:35], v[84:87], v[32:35], v[36:39]
	v_exp_f32_e32 v91, v55
	v_lshlrev_b32_e32 v52, 3, v185
	v_and_b32_e32 v208, 16, v52
	v_or_b32_e32 v36, 0x70, v184
	v_sub_u32_e32 v55, v133, v36
	v_sub_u32_e32 v36, 0, v55
	v_max_i32_e32 v36, v55, v36
	v_cvt_f32_u32_e32 v57, v36
	v_cmp_gt_i32_e32 vcc, 0, v55
	v_or_b32_e32 v55, 0x71, v184
	ds_read2_b64 v[36:39], v53 offset0:216 offset1:220
	v_cndmask_b32_e32 v53, v204, v132, vcc
	v_sub_u32_e32 v55, v133, v55
	v_mul_f32_e32 v53, v53, v57
	v_sub_u32_e32 v57, 0, v55
	v_max_i32_e32 v57, v55, v57
	v_cvt_f32_u32_e32 v57, v57
	v_cmp_gt_i32_e32 vcc, 0, v55
	v_or_b32_e32 v55, 0x72, v184
	v_exp_f32_e32 v70, v53
	v_cndmask_b32_e32 v53, v204, v132, vcc
	v_sub_u32_e32 v55, v133, v55
	v_mul_f32_e32 v53, v53, v57
	v_sub_u32_e32 v57, 0, v55
	v_max_i32_e32 v57, v55, v57
	v_cvt_f32_u32_e32 v57, v57
	v_cmp_gt_i32_e32 vcc, 0, v55
	v_or_b32_e32 v55, 0x73, v184
	v_exp_f32_e32 v71, v53
	v_cndmask_b32_e32 v53, v204, v132, vcc
	v_sub_u32_e32 v55, v133, v55
	v_mul_f32_e32 v53, v53, v57
	v_sub_u32_e32 v57, 0, v55
	v_max_i32_e32 v57, v55, v57
	v_cvt_f32_u32_e32 v57, v57
	v_cmp_gt_i32_e32 vcc, 0, v55
	s_waitcnt lgkmcnt(0)
; __device__ __forceinline__ void unit(const bf16_t* __restrict__ proj, const float* __restrict__ rope, const float* __restrict__ log_decay, const float* __restrict__ gn_g, bf16_t* __restrict__ ymix, ...
;     ...
;         f32x4 yacc[8];
; #pragma unroll
;         for (int mbv = 0; mbv < 8; ++mbv) {
;             f32x4 y = (f32x4){0.f, 0.f, 0.f, 0.f};
; #pragma unroll
;             for (int rep = 0; rep < (RET_PROBE == 1 ? 2 : 1); ++rep) {
;             unsigned zo = 0; if (RET_PROBE == 1) asm volatile("" : "+v"(zo));
; #pragma unroll
;             for (int ks2 = 0; ks2 < 4; ++ks2) y = __builtin_amdgcn_mfma_f32_16x16x32_bf16(trfrag(lds + LV + zo, 32 * ks2 + 4 * g, 32 * ks2 + 16 + 4 * g, mbv, qp, p), pt[ks2], y, 0, 0, 0);
; #pragma unroll
;             for (int ks = 0; ks < 4; ++ks) {
;                 y = __builtin_amdgcn_mfma_f32_16x16x32_bf16(trfrag(lds + LRF + zo, 32 * ks + 4 * g, 32 * ks + 16 + 4 * g, mbv, qp, p), qf[ks], y, 0, 0, 0);
;                 y = __builtin_amdgcn_mfma_f32_16x16x32_bf16(trfrag(lds + LRB + zo, 32 * ks + 4 * g, 32 * ks + 16 + 4 * g, mbv, qp, p), qb[ks], y, 0, 0, 0);
;             }
;             }
;             yacc[mbv] = (RET_PROBE == 1) ? y * 0.5f : y;
;         }
	v_mfma_f32_16x16x32_bf16 v[32:35], v[36:39], v[40:43], v[32:35]
	v_mul_f32_e64 v46, v90, v72
	v_mul_f32_e64 v47, v91, v73
	v_exp_f32_e32 v72, v53
	v_cndmask_b32_e32 v53, v204, v132, vcc
	v_mul_f32_e32 v53, v53, v57
	v_exp_f32_e32 v73, v53
	s_nop 1
	v_pk_mul_f32 v[36:37], v[70:71], v[32:33]
	v_or_b32_e32 v33, v184, v123
	v_and_b32_e32 v207, 8, v52
	v_add_u32_e32 v32, 0, v208
	v_mul_u32_u24_e32 v209, 0x120, v33
	v_add3_u32 v205, v32, v207, v209
	v_pk_mul_f32 v[38:39], v[72:73], v[34:35]
	ds_read_b64_tr_b16 v[34:35], v205 offset:41472
	ds_read_b64_tr_b16 v[32:33], v205 offset:36864
	v_cvt_pk_bf16_f32 v166, v36, v37
	v_cvt_pk_bf16_f32 v167, v38, v39
	ds_read_b64_tr_b16 v[36:37], v205 offset:46080
	ds_read_b64_tr_b16 v[38:39], v205 offset:50688
	s_waitcnt lgkmcnt(2)
	v_mfma_f32_16x16x32_bf16 v[32:35], v[32:35], v[156:159], 0
	ds_read_b64_tr_b16 v[40:41], v205 offset:55296
	ds_read_b64_tr_b16 v[42:43], v205 offset:59904
	s_add_i32 s8, s5, -1
	v_cvt_pk_bf16_f32 v165, v46, v47
	s_waitcnt lgkmcnt(2)
	v_mfma_f32_16x16x32_bf16 v[32:35], v[36:39], v[168:171], v[32:35]
	v_add_u32_e32 v46, 0xfc00, v205
	s_cmp_lt_u32 s5, s75
	v_cvt_pk_bf16_f32 v154, v92, v93
	v_cvt_pk_bf16_f32 v155, v94, v95
	v_cvt_pk_bf16_f32 v164, v44, v45
	ds_read_b64_tr_b16 v[44:45], v205 offset:64512
	ds_read_b64_tr_b16 v[46:47], v46 offset:4608
	s_cselect_b32 s8, s5, s8
	s_add_i32 s9, 0, 0x12000
	s_waitcnt lgkmcnt(2)
	v_mfma_f32_16x16x32_bf16 v[32:35], v[40:43], v[152:155], v[32:35]
	v_add_u32_e32 v53, s9, v208
	v_add3_u32 v210, v53, v207, v209
	ds_read_b64_tr_b16 v[38:39], v210 offset:4608
	ds_read_b64_tr_b16 v[36:37], v210
	s_add_i32 s85, 0, 0x1b000
	s_waitcnt lgkmcnt(2)
	v_mfma_f32_16x16x32_bf16 v[32:35], v[44:47], v[164:167], v[32:35]
	v_add_u32_e32 v55, s85, v208
	v_add3_u32 v176, v55, v207, v209
	ds_read_b64_tr_b16 v[42:43], v176 offset:4608
	ds_read_b64_tr_b16 v[40:41], v176
	s_waitcnt lgkmcnt(2)
	v_mfma_f32_16x16x32_bf16 v[32:35], v[36:39], v[116:119], v[32:35]
	ds_read_b64_tr_b16 v[44:45], v210 offset:9216
	ds_read_b64_tr_b16 v[46:47], v210 offset:13824
	ds_read_b64_tr_b16 v[36:37], v176 offset:9216
	ds_read_b64_tr_b16 v[38:39], v176 offset:13824
	v_cvt_pk_bf16_f32 v160, v62, v63
	s_waitcnt lgkmcnt(4)
	v_mfma_f32_16x16x32_bf16 v[32:35], v[40:43], v[128:131], v[32:35]
	v_cvt_pk_bf16_f32 v161, v66, v67
	v_cvt_pk_bf16_f32 v162, v50, v51
	ds_read_b64_tr_b16 v[40:41], v210 offset:18432
	ds_read_b64_tr_b16 v[42:43], v210 offset:23040
	s_waitcnt lgkmcnt(4)
	v_mfma_f32_16x16x32_bf16 v[32:35], v[44:47], v[136:139], v[32:35]
	v_cvt_pk_bf16_f32 v163, v48, v49
	ds_read_b64_tr_b16 v[44:45], v176 offset:18432
	ds_read_b64_tr_b16 v[46:47], v176 offset:23040
	v_pk_mul_f32 v[48:49], v[56:57], v[68:69] op_sel_hi:[0,1]
	s_waitcnt lgkmcnt(4)
	v_mfma_f32_16x16x32_bf16 v[32:35], v[36:39], v[160:163], v[32:35]
	ds_read_b64_tr_b16 v[36:37], v210 offset:27648
	ds_read_b64_tr_b16 v[38:39], v210 offset:32256
	v_cvt_pk_bf16_f32 v123, v48, v49
	v_cvt_pk_bf16_f32 v148, v58, v59
	s_waitcnt lgkmcnt(4)
	v_mfma_f32_16x16x32_bf16 v[32:35], v[40:43], v[108:111], v[32:35]
	ds_read_b64_tr_b16 v[40:41], v176 offset:27648
	ds_read_b64_tr_b16 v[42:43], v176 offset:32256
	v_cvt_pk_bf16_f32 v149, v60, v61
	v_cvt_pk_bf16_f32 v150, v64, v65
	s_waitcnt lgkmcnt(4)
	v_mfma_f32_16x16x32_bf16 v[32:35], v[44:47], v[124:127], v[32:35]
	v_mul_f32_e64 v44, v54, v68
	v_mul_f32_e64 v45, v54, v69
	v_cvt_pk_bf16_f32 v151, v44, v45
	s_lshl_b32 s85, s8, 7
	s_waitcnt lgkmcnt(2)
	v_mfma_f32_16x16x32_bf16 v[32:35], v[36:39], v[120:123], v[32:35]
	v_and_b32_e32 v46, 56, v52
	s_waitcnt lgkmcnt(0)
	v_mfma_f32_16x16x32_bf16 v[144:147], v[40:43], v[148:151], v[32:35]
	v_lshlrev_b32_e32 v44, 2, v46
	v_mov_b32_e32 v45, v177
	v_add_u32_e32 v50, s85, v74
	ds_read_b64_tr_b16 v[222:223], v205 offset:36896
	ds_read_b64_tr_b16 v[224:225], v205 offset:41504
	ds_read_b64_tr_b16 v[226:227], v205 offset:46112
	ds_read_b64_tr_b16 v[228:229], v205 offset:50720
	ds_read_b64_tr_b16 v[236:237], v205 offset:55328
	ds_read_b64_tr_b16 v[238:239], v205 offset:59936
	s_waitcnt lgkmcnt(4)
	v_mfma_f32_16x16x32_bf16 v[32:35], v[222:225], v[156:159], 0
	v_lshl_add_u64 v[52:53], s[20:21], 0, v[44:45]
	v_lshl_add_u64 v[60:61], s[14:15], 0, v[44:45]
	s_waitcnt lgkmcnt(2)
	v_mfma_f32_16x16x32_bf16 v[32:35], v[226:229], v[168:171], v[32:35]
	v_add_u32_e32 v44, s76, v50
	v_mad_i64_i32 v[44:45], s[8:9], v44, s67, v[98:99]
	s_waitcnt lgkmcnt(0)
	v_mfma_f32_16x16x32_bf16 v[32:35], v[236:239], v[152:155], v[32:35]
	v_add_u32_e32 v38, 0xfc20, v205
	v_lshl_add_u64 v[44:45], v[44:45], 0, v[180:181]
	ds_read_b64_tr_b16 v[240:241], v205 offset:64544
	ds_read_b64_tr_b16 v[242:243], v38 offset:4608
	ds_read_b64_tr_b16 v[222:223], v210 offset:32
	ds_read_b64_tr_b16 v[224:225], v210 offset:4640
	ds_read_b64_tr_b16 v[226:227], v176 offset:32
	ds_read_b64_tr_b16 v[228:229], v176 offset:4640
	ds_read_b64_tr_b16 v[236:237], v210 offset:9248
	ds_read_b64_tr_b16 v[238:239], v210 offset:13856
	s_waitcnt lgkmcnt(6)
	v_mfma_f32_16x16x32_bf16 v[32:35], v[240:243], v[164:167], v[32:35]
	v_lshlrev_b32_e32 v46, 1, v46
	ds_read_b64_tr_b16 v[240:241], v176 offset:9248
	ds_read_b64_tr_b16 v[242:243], v176 offset:13856
	s_waitcnt lgkmcnt(6)
	v_mfma_f32_16x16x32_bf16 v[32:35], v[222:225], v[116:119], v[32:35]
	v_mov_b32_e32 v47, v177
	v_lshl_add_u64 v[44:45], v[44:45], 0, v[46:47]
	v_lshl_add_u64 v[48:49], v[44:45], 0, s[22:23]
	ds_read_b64_tr_b16 v[222:223], v210 offset:18464
	ds_read_b64_tr_b16 v[224:225], v210 offset:23072
	s_waitcnt lgkmcnt(6)
	v_mfma_f32_16x16x32_bf16 v[32:35], v[226:229], v[128:131], v[32:35]
	v_add_co_u32_e32 v44, vcc, s69, v44
	ds_read_b64_tr_b16 v[226:227], v176 offset:18464
	ds_read_b64_tr_b16 v[228:229], v176 offset:23072
	s_waitcnt lgkmcnt(6)
; __device__ __forceinline__ void unit(const bf16_t* __restrict__ proj, const float* __restrict__ rope, const float* __restrict__ log_decay, const float* __restrict__ gn_g, bf16_t* __restrict__ ymix, ...
;     ...
;         f32x4 yacc[8];
; #pragma unroll
;         for (int mbv = 0; mbv < 8; ++mbv) {
;             f32x4 y = (f32x4){0.f, 0.f, 0.f, 0.f};
; #pragma unroll
;             for (int rep = 0; rep < (RET_PROBE == 1 ? 2 : 1); ++rep) {
;             unsigned zo = 0; if (RET_PROBE == 1) asm volatile("" : "+v"(zo));
; #pragma unroll
;             for (int ks2 = 0; ks2 < 4; ++ks2) y = __builtin_amdgcn_mfma_f32_16x16x32_bf16(trfrag(lds + LV + zo, 32 * ks2 + 4 * g, 32 * ks2 + 16 + 4 * g, mbv, qp, p), pt[ks2], y, 0, 0, 0);
; #pragma unroll
;             for (int ks = 0; ks < 4; ++ks) {
;                 y = __builtin_amdgcn_mfma_f32_16x16x32_bf16(trfrag(lds + LRF + zo, 32 * ks + 4 * g, 32 * ks + 16 + 4 * g, mbv, qp, p), qf[ks], y, 0, 0, 0);
;                 y = __builtin_amdgcn_mfma_f32_16x16x32_bf16(trfrag(lds + LRB + zo, 32 * ks + 4 * g, 32 * ks + 16 + 4 * g, mbv, qp, p), qb[ks], y, 0, 0, 0);
;             }
;             }
;             yacc[mbv] = (RET_PROBE == 1) ? y * 0.5f : y;
;         }
	v_mfma_f32_16x16x32_bf16 v[32:35], v[236:239], v[136:139], v[32:35]
	v_addc_co_u32_e32 v45, vcc, 0, v45, vcc
	ds_read_b64_tr_b16 v[236:237], v210 offset:27680
	ds_read_b64_tr_b16 v[238:239], v210 offset:32288
	s_waitcnt lgkmcnt(6)
	v_mfma_f32_16x16x32_bf16 v[32:35], v[240:243], v[160:163], v[32:35]
	v_add_u32_e32 v56, s85, v188
	s_add_i32 s86, s85, s76
	ds_read_b64_tr_b16 v[240:241], v176 offset:27680
	ds_read_b64_tr_b16 v[242:243], v176 offset:32288
	s_waitcnt lgkmcnt(6)
	v_mfma_f32_16x16x32_bf16 v[32:35], v[222:225], v[108:111], v[32:35]
	v_add_u32_e32 v174, s86, v174
	v_mad_i64_i32 v[192:193], s[8:9], v174, s67, v[98:99]
	s_waitcnt lgkmcnt(4)
	v_mfma_f32_16x16x32_bf16 v[32:35], v[226:229], v[124:127], v[32:35]
	v_lshl_add_u64 v[192:193], v[192:193], 0, v[180:181]
	v_add_u32_e32 v174, s86, v175
	s_waitcnt lgkmcnt(2)
	v_mfma_f32_16x16x32_bf16 v[32:35], v[236:239], v[120:123], v[32:35]
	s_cmp_ge_u32 s5, s75
	s_waitcnt lgkmcnt(0)
	v_mfma_f32_16x16x32_bf16 v[112:115], v[240:243], v[148:151], v[32:35]
	s_nop 2
	ds_read_b64_tr_b16 v[32:33], v205 offset:36928
	ds_read_b64_tr_b16 v[34:35], v205 offset:41536
	ds_read_b64_tr_b16 v[36:37], v205 offset:46144
	ds_read_b64_tr_b16 v[38:39], v205 offset:50752
	ds_read_b64_tr_b16 v[40:41], v205 offset:55360
	ds_read_b64_tr_b16 v[42:43], v205 offset:59968
	s_waitcnt lgkmcnt(4)
	v_mfma_f32_16x16x32_bf16 v[32:35], v[32:35], v[156:159], 0
	s_waitcnt lgkmcnt(2)
	v_mfma_f32_16x16x32_bf16 v[32:35], v[36:39], v[168:171], v[32:35]
	v_add_u32_e32 v38, 0xfc40, v205
	ds_read_b64_tr_b16 v[36:37], v205 offset:64576
	ds_read_b64_tr_b16 v[38:39], v38 offset:4608
	s_waitcnt lgkmcnt(2)
	v_mfma_f32_16x16x32_bf16 v[32:35], v[40:43], v[152:155], v[32:35]
	ds_read_b64_tr_b16 v[40:41], v210 offset:64
	ds_read_b64_tr_b16 v[42:43], v210 offset:4672
	s_waitcnt lgkmcnt(2)
	v_mfma_f32_16x16x32_bf16 v[32:35], v[36:39], v[164:167], v[32:35]
	ds_read_b64_tr_b16 v[36:37], v176 offset:64
	ds_read_b64_tr_b16 v[38:39], v176 offset:4672
	s_waitcnt lgkmcnt(2)
	v_mfma_f32_16x16x32_bf16 v[32:35], v[40:43], v[116:119], v[32:35]
	ds_read_b64_tr_b16 v[40:41], v210 offset:9280
	ds_read_b64_tr_b16 v[42:43], v210 offset:13888
	s_waitcnt lgkmcnt(2)
	v_mfma_f32_16x16x32_bf16 v[32:35], v[36:39], v[128:131], v[32:35]
	ds_read_b64_tr_b16 v[36:37], v176 offset:9280
	ds_read_b64_tr_b16 v[38:39], v176 offset:13888
	s_waitcnt lgkmcnt(2)
	v_mfma_f32_16x16x32_bf16 v[32:35], v[40:43], v[136:139], v[32:35]
	ds_read_b64_tr_b16 v[40:41], v210 offset:18496
	ds_read_b64_tr_b16 v[42:43], v210 offset:23104
	s_waitcnt lgkmcnt(2)
	v_mfma_f32_16x16x32_bf16 v[32:35], v[36:39], v[160:163], v[32:35]
	ds_read_b64_tr_b16 v[36:37], v176 offset:18496
	ds_read_b64_tr_b16 v[38:39], v176 offset:23104
	s_waitcnt lgkmcnt(2)
	v_mfma_f32_16x16x32_bf16 v[32:35], v[40:43], v[108:111], v[32:35]
	ds_read_b64_tr_b16 v[40:41], v210 offset:27712
	ds_read_b64_tr_b16 v[42:43], v210 offset:32320
	s_waitcnt lgkmcnt(2)
	v_mfma_f32_16x16x32_bf16 v[32:35], v[36:39], v[124:127], v[32:35]
	ds_read_b64_tr_b16 v[36:37], v176 offset:27712
	ds_read_b64_tr_b16 v[38:39], v176 offset:32320
	s_waitcnt lgkmcnt(2)
	v_mfma_f32_16x16x32_bf16 v[32:35], v[40:43], v[120:123], v[32:35]
	ds_read_b64_tr_b16 v[40:41], v205 offset:36960
	ds_read_b64_tr_b16 v[42:43], v205 offset:41568
	s_waitcnt lgkmcnt(2)
	v_mfma_f32_16x16x32_bf16 v[140:143], v[36:39], v[148:151], v[32:35]
	s_nop 3
	ds_read_b64_tr_b16 v[32:33], v205 offset:46176
	ds_read_b64_tr_b16 v[34:35], v205 offset:50784
	s_waitcnt lgkmcnt(2)
	v_mfma_f32_16x16x32_bf16 v[36:39], v[40:43], v[156:159], 0
	ds_read_b64_tr_b16 v[40:41], v205 offset:55392
	ds_read_b64_tr_b16 v[42:43], v205 offset:60000
	s_waitcnt lgkmcnt(2)
	v_mfma_f32_16x16x32_bf16 v[32:35], v[32:35], v[168:171], v[36:39]
	s_nop 3
	v_add_u32_e32 v38, 0xfc60, v205
	ds_read_b64_tr_b16 v[36:37], v205 offset:64608
	ds_read_b64_tr_b16 v[38:39], v38 offset:4608
	s_waitcnt lgkmcnt(2)
	v_mfma_f32_16x16x32_bf16 v[32:35], v[40:43], v[152:155], v[32:35]
	ds_read_b64_tr_b16 v[40:41], v210 offset:96
	ds_read_b64_tr_b16 v[42:43], v210 offset:4704
	s_waitcnt lgkmcnt(2)
	v_mfma_f32_16x16x32_bf16 v[32:35], v[36:39], v[164:167], v[32:35]
	ds_read_b64_tr_b16 v[36:37], v176 offset:96
	ds_read_b64_tr_b16 v[38:39], v176 offset:4704
	s_waitcnt lgkmcnt(2)
	v_mfma_f32_16x16x32_bf16 v[32:35], v[40:43], v[116:119], v[32:35]
	ds_read_b64_tr_b16 v[40:41], v210 offset:9312
	ds_read_b64_tr_b16 v[42:43], v210 offset:13920
	s_waitcnt lgkmcnt(2)
	v_mfma_f32_16x16x32_bf16 v[32:35], v[36:39], v[128:131], v[32:35]
	ds_read_b64_tr_b16 v[36:37], v176 offset:9312
	ds_read_b64_tr_b16 v[38:39], v176 offset:13920
	s_waitcnt lgkmcnt(2)
	v_mfma_f32_16x16x32_bf16 v[32:35], v[40:43], v[136:139], v[32:35]
	ds_read_b64_tr_b16 v[40:41], v210 offset:18528
	ds_read_b64_tr_b16 v[42:43], v210 offset:23136
	s_waitcnt lgkmcnt(2)
	v_mfma_f32_16x16x32_bf16 v[32:35], v[36:39], v[160:163], v[32:35]
	ds_read_b64_tr_b16 v[36:37], v176 offset:18528
	ds_read_b64_tr_b16 v[38:39], v176 offset:23136
	s_waitcnt lgkmcnt(2)
	v_mfma_f32_16x16x32_bf16 v[32:35], v[40:43], v[108:111], v[32:35]
	ds_read_b64_tr_b16 v[40:41], v210 offset:27744
	ds_read_b64_tr_b16 v[42:43], v210 offset:32352
	s_waitcnt lgkmcnt(2)
	v_mfma_f32_16x16x32_bf16 v[32:35], v[36:39], v[124:127], v[32:35]
	ds_read_b64_tr_b16 v[36:37], v176 offset:27744
	ds_read_b64_tr_b16 v[38:39], v176 offset:32352
	s_waitcnt lgkmcnt(2)
	v_mfma_f32_16x16x32_bf16 v[32:35], v[40:43], v[120:123], v[32:35]
	ds_read_b64_tr_b16 v[40:41], v205 offset:36992
	ds_read_b64_tr_b16 v[42:43], v205 offset:41600
	s_waitcnt lgkmcnt(2)
; __device__ __forceinline__ void kv_load(KVRaw& R, const bf16_t* __restrict__ proj, const float* __restrict__ rope, int b, int h, int n, int tid) {
; #pragma unroll
;     for (int i = 0; i < 2; ++i) {
;         const int q2 = tid + 512 * i, row = q2 >> 3, pc = q2 & 7, t = n * 128 + row;
;         const bf16_t* rp = proj + (size_t)(b * SEQ + t) * DIN + OFF_KR + h * 128;
;         R.ka[i] = *(const bf16x8*)(rp + pc * 8); R.kb[i] = *(const bf16x8*)(rp + 64 + pc * 8);
;         R.c0[i] = *(const f32x4*)(rope + t * 64 + pc * 8); R.c1[i] = *(const f32x4*)(rope + t * 64 + pc * 8 + 4);
;         R.s0[i] = *(const f32x4*)(rope + SEQ * 64 + t * 64 + pc * 8); R.s1[i] = *(const f32x4*)(rope + SEQ * 64 + t * 64 + pc * 8 + 4);
;     }
; #pragma unroll
;     for (int i = 0; i < 4; ++i) { const int q4 = tid + 512 * i, row = q4 >> 4, ch = q4 & 15, t = n * 128 + row;
;         R.v[i] = *(const bf16x8*)(proj + (size_t)(b * SEQ + t) * DIN + OFF_VR + h * 128 + ch * 8); }
; __device__ __forceinline__ void unit(const bf16_t* __restrict__ proj, const float* __restrict__ rope, const float* __restrict__ log_decay, const float* __restrict__ gn_g, bf16_t* __restrict__ ymix, ...
;     ...
;         for (int mbv = 0; mbv < 8; ++mbv) {
;             f32x4 y = (f32x4){0.f, 0.f, 0.f, 0.f};
; #pragma unroll
;             for (int rep = 0; rep < (RET_PROBE == 1 ? 2 : 1); ++rep) {
;             unsigned zo = 0; if (RET_PROBE == 1) asm volatile("" : "+v"(zo));
; #pragma unroll
;             for (int ks2 = 0; ks2 < 4; ++ks2) y = __builtin_amdgcn_mfma_f32_16x16x32_bf16(trfrag(lds + LV + zo, 32 * ks2 + 4 * g, 32 * ks2 + 16 + 4 * g, mbv, qp, p), pt[ks2], y, 0, 0, 0);
; #pragma unroll
;             for (int ks = 0; ks < 4; ++ks) {
;                 y = __builtin_amdgcn_mfma_f32_16x16x32_bf16(trfrag(lds + LRF + zo, 32 * ks + 4 * g, 32 * ks + 16 + 4 * g, mbv, qp, p), qf[ks], y, 0, 0, 0);
;                 y = __builtin_amdgcn_mfma_f32_16x16x32_bf16(trfrag(lds + LRB + zo, 32 * ks + 4 * g, 32 * ks + 16 + 4 * g, mbv, qp, p), qb[ks], y, 0, 0, 0);
;             }
	v_mfma_f32_16x16x32_bf16 v[132:135], v[36:39], v[148:151], v[32:35]
	s_nop 3
	ds_read_b64_tr_b16 v[32:33], v205 offset:46208
	ds_read_b64_tr_b16 v[34:35], v205 offset:50816
	global_load_dwordx4 v[76:79], v[44:45], off
	v_lshlrev_b32_e32 v44, 6, v50
	s_waitcnt lgkmcnt(2)
	v_mfma_f32_16x16x32_bf16 v[36:39], v[40:43], v[156:159], 0
	ds_read_b64_tr_b16 v[40:41], v205 offset:55424
	ds_read_b64_tr_b16 v[42:43], v205 offset:60032
	global_load_dwordx4 v[72:75], v[48:49], off offset:128
	v_ashrrev_i32_e32 v45, 31, v44
	s_waitcnt lgkmcnt(2)
	v_mfma_f32_16x16x32_bf16 v[32:35], v[32:35], v[168:171], v[36:39]
	v_lshlrev_b64 v[44:45], 2, v[44:45]
	v_lshl_add_u64 v[48:49], v[52:53], 0, v[44:45]
	v_lshl_add_u64 v[44:45], v[60:61], 0, v[44:45]
	v_add_u32_e32 v38, 0xfc80, v205
	ds_read_b64_tr_b16 v[36:37], v205 offset:64640
	ds_read_b64_tr_b16 v[38:39], v38 offset:4608
	s_waitcnt lgkmcnt(2)
	v_mfma_f32_16x16x32_bf16 v[32:35], v[40:43], v[152:155], v[32:35]
	ds_read_b64_tr_b16 v[40:41], v210 offset:128
	ds_read_b64_tr_b16 v[42:43], v210 offset:4736
	global_load_dwordx4 v[80:83], v[48:49], off offset:16
	global_load_dwordx4 v[88:91], v[48:49], off
	s_waitcnt lgkmcnt(2)
	v_mfma_f32_16x16x32_bf16 v[32:35], v[36:39], v[164:167], v[32:35]
	ds_read_b64_tr_b16 v[36:37], v176 offset:128
	ds_read_b64_tr_b16 v[38:39], v176 offset:4736
	global_load_dwordx4 v[84:87], v[44:45], off offset:16
	s_waitcnt lgkmcnt(2)
	v_mfma_f32_16x16x32_bf16 v[32:35], v[40:43], v[116:119], v[32:35]
	ds_read_b64_tr_b16 v[40:41], v210 offset:9344
	ds_read_b64_tr_b16 v[42:43], v210 offset:13952
	global_load_dwordx4 v[92:95], v[44:45], off
	v_add_u32_e32 v44, s76, v56
	s_waitcnt lgkmcnt(2)
	v_mfma_f32_16x16x32_bf16 v[32:35], v[36:39], v[128:131], v[32:35]
	ds_read_b64_tr_b16 v[36:37], v176 offset:9344
	ds_read_b64_tr_b16 v[38:39], v176 offset:13952
	v_mad_i64_i32 v[44:45], s[8:9], v44, s67, v[98:99]
	s_waitcnt lgkmcnt(2)
	v_mfma_f32_16x16x32_bf16 v[32:35], v[40:43], v[136:139], v[32:35]
	ds_read_b64_tr_b16 v[40:41], v210 offset:18560
	ds_read_b64_tr_b16 v[42:43], v210 offset:23168
	v_lshl_add_u64 v[44:45], v[44:45], 0, v[180:181]
	v_lshl_add_u64 v[44:45], v[44:45], 0, v[46:47]
	s_waitcnt lgkmcnt(2)
	v_mfma_f32_16x16x32_bf16 v[32:35], v[36:39], v[160:163], v[32:35]
	ds_read_b64_tr_b16 v[36:37], v176 offset:18560
	ds_read_b64_tr_b16 v[38:39], v176 offset:23168
	ds_read_b64_tr_b16 v[48:49], v210 offset:27776
	ds_read_b64_tr_b16 v[50:51], v210 offset:32384
	v_lshl_add_u64 v[54:55], v[44:45], 0, s[22:23]
	s_waitcnt lgkmcnt(4)
	v_mfma_f32_16x16x32_bf16 v[32:35], v[40:43], v[108:111], v[32:35]
	v_add_co_u32_e32 v44, vcc, s69, v44
	s_waitcnt lgkmcnt(2)
	v_mfma_f32_16x16x32_bf16 v[32:35], v[36:39], v[124:127], v[32:35]
	v_addc_co_u32_e32 v45, vcc, 0, v45, vcc
	global_load_dwordx4 v[44:47], v[44:45], off
	ds_read_b64_tr_b16 v[36:37], v176 offset:27776
	ds_read_b64_tr_b16 v[38:39], v176 offset:32384
	global_load_dwordx4 v[40:43], v[54:55], off offset:128
	s_waitcnt lgkmcnt(2)
	v_mfma_f32_16x16x32_bf16 v[32:35], v[48:51], v[120:123], v[32:35]
	ds_read_b64_tr_b16 v[48:49], v205 offset:37024
	ds_read_b64_tr_b16 v[50:51], v205 offset:41632
	v_lshlrev_b32_e32 v54, 6, v56
	v_ashrrev_i32_e32 v55, 31, v54
	v_lshlrev_b64 v[62:63], 2, v[54:55]
	v_lshl_add_u64 v[56:57], v[52:53], 0, v[62:63]
	ds_read_b64_tr_b16 v[52:53], v205 offset:46240
	ds_read_b64_tr_b16 v[54:55], v205 offset:50848
	s_waitcnt lgkmcnt(2)
	v_mfma_f32_16x16x32_bf16 v[48:51], v[48:51], v[156:159], 0
	v_lshl_add_u64 v[60:61], v[60:61], 0, v[62:63]
	v_mfma_f32_16x16x32_bf16 v[104:107], v[36:39], v[148:151], v[32:35]
	s_nop 2
	global_load_dwordx4 v[32:35], v[56:57], off offset:16
	global_load_dwordx4 v[64:67], v[56:57], off
	ds_read_b64_tr_b16 v[56:57], v205 offset:55456
	ds_read_b64_tr_b16 v[58:59], v205 offset:60064
	global_load_dwordx4 v[36:39], v[60:61], off offset:16
	global_load_dwordx4 v[68:71], v[60:61], off
	s_waitcnt lgkmcnt(2)
	v_mfma_f32_16x16x32_bf16 v[48:51], v[52:55], v[168:171], v[48:51]
	v_add_u32_e32 v54, 0xfca0, v205
	ds_read_b64_tr_b16 v[52:53], v205 offset:64672
	ds_read_b64_tr_b16 v[54:55], v54 offset:4608
	v_add_u32_e32 v60, s86, v173
	s_waitcnt lgkmcnt(2)
	v_mfma_f32_16x16x32_bf16 v[48:51], v[56:59], v[152:155], v[48:51]
	ds_read_b64_tr_b16 v[56:57], v210 offset:160
	ds_read_b64_tr_b16 v[58:59], v210 offset:4768
	v_mad_i64_i32 v[60:61], s[8:9], v60, s67, v[98:99]
	s_waitcnt lgkmcnt(2)
	v_mfma_f32_16x16x32_bf16 v[48:51], v[52:55], v[164:167], v[48:51]
	ds_read_b64_tr_b16 v[52:53], v176 offset:160
	ds_read_b64_tr_b16 v[54:55], v176 offset:4768
	v_lshl_add_u64 v[60:61], v[60:61], 0, v[180:181]
	v_mov_b32_e32 v173, v177
	s_waitcnt lgkmcnt(2)
	v_mfma_f32_16x16x32_bf16 v[48:51], v[56:59], v[116:119], v[48:51]
	ds_read_b64_tr_b16 v[56:57], v210 offset:9376
	ds_read_b64_tr_b16 v[58:59], v210 offset:13984
	v_lshl_add_u64 v[100:101], v[60:61], 0, v[172:173]
	ds_read_b64_tr_b16 v[60:61], v176 offset:9376
	ds_read_b64_tr_b16 v[62:63], v176 offset:13984
	s_waitcnt lgkmcnt(4)
	v_mfma_f32_16x16x32_bf16 v[52:55], v[52:55], v[128:131], v[48:51]
	v_add_co_u32_e32 v100, vcc, s69, v100
	v_lshl_add_u64 v[192:193], v[192:193], 0, v[172:173]
	s_waitcnt lgkmcnt(2)
	v_mfma_f32_16x16x32_bf16 v[52:55], v[56:59], v[136:139], v[52:55]
	v_addc_co_u32_e32 v101, vcc, 0, v101, vcc
	global_load_dwordx4 v[48:51], v[100:101], off offset:1024
	ds_read_b64_tr_b16 v[56:57], v210 offset:18592
	ds_read_b64_tr_b16 v[58:59], v210 offset:23200
	s_waitcnt lgkmcnt(2)
	v_mfma_f32_16x16x32_bf16 v[52:55], v[60:63], v[160:163], v[52:55]
	ds_read_b64_tr_b16 v[60:61], v176 offset:18592
	ds_read_b64_tr_b16 v[62:63], v176 offset:23200
	v_add_u32_e32 v100, s86, v187
	v_mad_i64_i32 v[100:101], s[8:9], v100, s67, v[98:99]
	s_waitcnt lgkmcnt(2)
; __device__ __forceinline__ void unit(const bf16_t* __restrict__ proj, const float* __restrict__ rope, const float* __restrict__ log_decay, const float* __restrict__ gn_g, bf16_t* __restrict__ ymix, ...
;     ...
;         u32x2 gv[8];
;         { const bf16_t* gp = proj + (size_t)(b * SEQ + tq) * DIN + OFF_GR + h * 128 + 4 * g;
; #pragma unroll
;           for (int mbv = 0; mbv < 8; ++mbv) gv[mbv] = *(const u32x2*)(gp + 16 * mbv); }
;     ...
;         for (int mbv = 0; mbv < 8; ++mbv) {
;             f32x4 y = (f32x4){0.f, 0.f, 0.f, 0.f};
; #pragma unroll
;             for (int rep = 0; rep < (RET_PROBE == 1 ? 2 : 1); ++rep) {
;             unsigned zo = 0; if (RET_PROBE == 1) asm volatile("" : "+v"(zo));
; #pragma unroll
;             for (int ks2 = 0; ks2 < 4; ++ks2) y = __builtin_amdgcn_mfma_f32_16x16x32_bf16(trfrag(lds + LV + zo, 32 * ks2 + 4 * g, 32 * ks2 + 16 + 4 * g, mbv, qp, p), pt[ks2], y, 0, 0, 0);
; #pragma unroll
;             for (int ks = 0; ks < 4; ++ks) {
;                 y = __builtin_amdgcn_mfma_f32_16x16x32_bf16(trfrag(lds + LRF + zo, 32 * ks + 4 * g, 32 * ks + 16 + 4 * g, mbv, qp, p), qf[ks], y, 0, 0, 0);
;                 y = __builtin_amdgcn_mfma_f32_16x16x32_bf16(trfrag(lds + LRB + zo, 32 * ks + 4 * g, 32 * ks + 16 + 4 * g, mbv, qp, p), qb[ks], y, 0, 0, 0);
;             }
;             }
;             yacc[mbv] = (RET_PROBE == 1) ? y * 0.5f : y;
;         }
;         __syncthreads();
	v_mfma_f32_16x16x32_bf16 v[52:55], v[56:59], v[108:111], v[52:55]
	ds_read_b64_tr_b16 v[56:57], v210 offset:27808
	ds_read_b64_tr_b16 v[58:59], v210 offset:32416
	v_lshl_add_u64 v[100:101], v[100:101], 0, v[180:181]
	v_lshl_add_u64 v[100:101], v[100:101], 0, v[172:173]
	s_waitcnt lgkmcnt(2)
	v_mfma_f32_16x16x32_bf16 v[52:55], v[60:63], v[124:127], v[52:55]
	ds_read_b64_tr_b16 v[60:61], v176 offset:27808
	ds_read_b64_tr_b16 v[62:63], v176 offset:32416
	ds_read_b64_tr_b16 v[188:189], v205 offset:37056
	ds_read_b64_tr_b16 v[190:191], v205 offset:41664
	v_add_co_u32_e32 v100, vcc, s69, v100
	s_waitcnt lgkmcnt(4)
	v_mfma_f32_16x16x32_bf16 v[56:59], v[56:59], v[120:123], v[52:55]
	v_addc_co_u32_e32 v101, vcc, 0, v101, vcc
	v_add_u32_e32 v187, 0xfcc0, v205
	s_nop 0
	global_load_dwordx4 v[52:55], v[100:101], off offset:1024
	ds_read_b64_tr_b16 v[212:213], v205 offset:46272
	ds_read_b64_tr_b16 v[214:215], v205 offset:50880
	s_waitcnt lgkmcnt(4)
	v_mfma_f32_16x16x32_bf16 v[100:103], v[60:63], v[148:151], v[56:59]
	s_nop 2
	ds_read_b64_tr_b16 v[56:57], v205 offset:55488
	ds_read_b64_tr_b16 v[58:59], v205 offset:60096
	v_add_co_u32_e32 v192, vcc, s69, v192
	s_waitcnt lgkmcnt(4)
	v_mfma_f32_16x16x32_bf16 v[60:63], v[188:191], v[156:159], 0
	ds_read_b64_tr_b16 v[188:189], v205 offset:64704
	ds_read_b64_tr_b16 v[190:191], v187 offset:4608
	v_addc_co_u32_e32 v193, vcc, 0, v193, vcc
	s_waitcnt lgkmcnt(4)
	v_mfma_f32_16x16x32_bf16 v[60:63], v[212:215], v[168:171], v[60:63]
	v_mad_i64_i32 v[98:99], s[8:9], v174, s67, v[98:99]
	v_lshl_add_u64 v[98:99], v[98:99], 0, v[180:181]
	s_waitcnt lgkmcnt(2)
	v_mfma_f32_16x16x32_bf16 v[56:59], v[56:59], v[152:155], v[60:63]
	s_nop 3
	ds_read_b64_tr_b16 v[60:61], v210 offset:192
	ds_read_b64_tr_b16 v[62:63], v210 offset:4800
	v_lshl_add_u64 v[98:99], v[98:99], 0, v[172:173]
	v_add_co_u32_e32 v98, vcc, s69, v98
	s_waitcnt lgkmcnt(2)
	v_mfma_f32_16x16x32_bf16 v[56:59], v[188:191], v[164:167], v[56:59]
	ds_read_b64_tr_b16 v[188:189], v176 offset:192
	ds_read_b64_tr_b16 v[190:191], v176 offset:4800
	ds_read_b64_tr_b16 v[212:213], v210 offset:9408
	ds_read_b64_tr_b16 v[214:215], v210 offset:14016
	v_addc_co_u32_e32 v99, vcc, 0, v99, vcc
	s_waitcnt lgkmcnt(4)
	v_mfma_f32_16x16x32_bf16 v[56:59], v[60:63], v[116:119], v[56:59]
	global_load_dwordx4 v[60:63], v[192:193], off offset:1024
	v_add_co_u32_e32 v220, vcc, s69, v96
	s_waitcnt lgkmcnt(2)
	v_mfma_f32_16x16x32_bf16 v[56:59], v[188:191], v[128:131], v[56:59]
	ds_read_b64_tr_b16 v[188:189], v176 offset:9408
	ds_read_b64_tr_b16 v[190:191], v176 offset:14016
	v_addc_co_u32_e32 v221, vcc, 0, v97, vcc
	s_waitcnt lgkmcnt(2)
	v_mfma_f32_16x16x32_bf16 v[56:59], v[212:215], v[136:139], v[56:59]
	ds_read_b64_tr_b16 v[212:213], v210 offset:18624
	ds_read_b64_tr_b16 v[214:215], v210 offset:23232
	ds_read_b64_tr_b16 v[172:173], v176 offset:18624
	ds_read_b64_tr_b16 v[174:175], v176 offset:23232
	v_lshl_add_u64 v[192:193], v[96:97], 0, s[36:37]
	s_waitcnt lgkmcnt(4)
	v_mfma_f32_16x16x32_bf16 v[56:59], v[188:191], v[160:163], v[56:59]
	s_waitcnt lgkmcnt(2)
	v_mfma_f32_16x16x32_bf16 v[188:191], v[212:215], v[108:111], v[56:59]
	ds_read_b64_tr_b16 v[212:213], v210 offset:27840
	ds_read_b64_tr_b16 v[214:215], v210 offset:32448
	s_nop 3
	global_load_dwordx4 v[56:59], v[98:99], off offset:1024
	s_waitcnt lgkmcnt(2)
	v_mfma_f32_16x16x32_bf16 v[172:175], v[172:175], v[124:127], v[188:191]
	s_nop 2
	ds_read_b64_tr_b16 v[188:189], v176 offset:27840
	ds_read_b64_tr_b16 v[190:191], v176 offset:32448
	s_waitcnt lgkmcnt(2)
	v_mfma_f32_16x16x32_bf16 v[172:175], v[212:215], v[120:123], v[172:175]
	ds_read_b64_tr_b16 v[212:213], v205 offset:37088
	ds_read_b64_tr_b16 v[214:215], v205 offset:41696
	ds_read_b64_tr_b16 v[216:217], v205 offset:46304
	ds_read_b64_tr_b16 v[218:219], v205 offset:50912
	s_waitcnt lgkmcnt(2)
	v_mfma_f32_16x16x32_bf16 v[212:215], v[212:215], v[156:159], 0
	v_add_u32_e32 v158, 0xfce0, v205
	v_mfma_f32_16x16x32_bf16 v[96:99], v[188:191], v[148:151], v[172:175]
	global_load_dwordx2 v[190:191], v[220:221], off offset:2048
	s_nop 1
	ds_read_b64_tr_b16 v[172:173], v205 offset:55520
	ds_read_b64_tr_b16 v[174:175], v205 offset:60128
	ds_read_b64_tr_b16 v[156:157], v205 offset:64736
	ds_read_b64_tr_b16 v[158:159], v158 offset:4608
	s_waitcnt lgkmcnt(4)
	v_mfma_f32_16x16x32_bf16 v[168:171], v[216:219], v[168:171], v[212:215]
	global_load_dwordx2 v[188:189], v[192:193], off offset:32
	s_nop 1
	ds_read_b64_tr_b16 v[212:213], v210 offset:224
	ds_read_b64_tr_b16 v[214:215], v210 offset:4832
	s_waitcnt lgkmcnt(4)
	v_mfma_f32_16x16x32_bf16 v[152:155], v[172:175], v[152:155], v[168:171]
	global_load_dwordx2 v[172:173], v[192:193], off offset:64
	s_nop 1
	global_load_dwordx2 v[170:171], v[192:193], off offset:96
	global_load_dwordx2 v[168:169], v[192:193], off offset:128
	s_waitcnt lgkmcnt(2)
	v_mfma_f32_16x16x32_bf16 v[164:167], v[156:159], v[164:167], v[152:155]
	global_load_dwordx2 v[156:157], v[192:193], off offset:160
	s_nop 1
	global_load_dwordx2 v[154:155], v[192:193], off offset:192
	global_load_dwordx2 v[152:153], v[192:193], off offset:224
	s_waitcnt lgkmcnt(0)
	v_mfma_f32_16x16x32_bf16 v[116:119], v[212:215], v[116:119], v[164:167]
	s_nop 2
	ds_read_b64_tr_b16 v[164:165], v176 offset:224
	ds_read_b64_tr_b16 v[166:167], v176 offset:4832
	s_waitcnt lgkmcnt(0)
	v_mfma_f32_16x16x32_bf16 v[116:119], v[164:167], v[128:131], v[116:119]
	ds_read_b64_tr_b16 v[128:129], v210 offset:9440
	ds_read_b64_tr_b16 v[130:131], v210 offset:14048
	s_waitcnt lgkmcnt(0)
	v_mfma_f32_16x16x32_bf16 v[116:119], v[128:131], v[136:139], v[116:119]
	ds_read_b64_tr_b16 v[128:129], v176 offset:9440
	ds_read_b64_tr_b16 v[130:131], v176 offset:14048
	s_waitcnt lgkmcnt(0)
	v_mfma_f32_16x16x32_bf16 v[116:119], v[128:131], v[160:163], v[116:119]
	ds_read_b64_tr_b16 v[128:129], v210 offset:18656
	ds_read_b64_tr_b16 v[130:131], v210 offset:23264
	s_waitcnt lgkmcnt(0)
	v_mfma_f32_16x16x32_bf16 v[108:111], v[128:131], v[108:111], v[116:119]
	s_nop 3
	ds_read_b64_tr_b16 v[116:117], v176 offset:18656
	ds_read_b64_tr_b16 v[118:119], v176 offset:23264
	s_waitcnt lgkmcnt(0)
	v_mfma_f32_16x16x32_bf16 v[108:111], v[116:119], v[124:127], v[108:111]
	ds_read_b64_tr_b16 v[116:117], v210 offset:27872
	ds_read_b64_tr_b16 v[118:119], v210 offset:32480
	s_waitcnt lgkmcnt(0)
	v_mfma_f32_16x16x32_bf16 v[108:111], v[116:119], v[120:123], v[108:111]
	ds_read_b64_tr_b16 v[116:117], v176 offset:27872
	ds_read_b64_tr_b16 v[118:119], v176 offset:32480
	s_waitcnt lgkmcnt(0)
	s_barrier
	v_mfma_f32_16x16x32_bf16 v[108:111], v[116:119], v[148:151], v[108:111]
	s_cbranch_scc1 .LBB0_300
	v_and_b32_e32 v116, 63, v185
	s_andn2_b64 vcc, exec, s[40:41]
	v_lshlrev_b32_e32 v176, 4, v116
	s_cbranch_vccz .LBB0_307
	s_andn2_b64 vcc, exec, s[46:47]
	s_cbranch_vccz .LBB0_308
